# router logit reduce-scatter: first two stages via permlane32/16 swap of the partial registers + add (no selects, no LDS), remaining lane exchanges via DPP
# speedup vs baseline: 1.0050x; 1.0050x over previous
.LBB0_763:
	s_waitcnt vmcnt(4)
	v_lshlrev_b32_e32 v98, 16, v72
	v_and_b32_e32 v99, 0xffff0000, v72
	v_lshlrev_b32_e32 v72, 16, v73
	v_and_b32_e32 v73, 0xffff0000, v73
	v_lshlrev_b32_e32 v102, 16, v64
	v_and_b32_e32 v103, 0xffff0000, v64
	v_lshlrev_b32_e32 v64, 16, v65
	v_and_b32_e32 v65, 0xffff0000, v65
	v_lshlrev_b32_e32 v90, 16, v76
	v_and_b32_e32 v91, 0xffff0000, v76
	v_lshlrev_b32_e32 v76, 16, v77
	v_and_b32_e32 v77, 0xffff0000, v77
	v_lshlrev_b32_e32 v94, 16, v68
	v_and_b32_e32 v95, 0xffff0000, v68
	v_lshlrev_b32_e32 v68, 16, v69
	v_and_b32_e32 v69, 0xffff0000, v69
	v_lshlrev_b32_e32 v100, 16, v74
	v_and_b32_e32 v101, 0xffff0000, v74
	v_lshlrev_b32_e32 v74, 16, v75
	v_and_b32_e32 v75, 0xffff0000, v75
	v_lshlrev_b32_e32 v104, 16, v66
	v_and_b32_e32 v105, 0xffff0000, v66
	s_waitcnt vmcnt(1)
	v_pk_mul_f32 v[98:99], v[32:33], v[98:99]
	v_pk_mul_f32 v[72:73], v[34:35], v[72:73]
	s_mov_b32 s2, 0x3fd744fd
	v_pk_mul_f32 v[64:65], v[6:7], v[64:65]
	v_lshlrev_b32_e32 v92, 16, v78
	v_and_b32_e32 v93, 0xffff0000, v78
	v_lshlrev_b32_e32 v78, 16, v79
	v_and_b32_e32 v79, 0xffff0000, v79
	v_lshlrev_b32_e32 v96, 16, v70
	v_and_b32_e32 v97, 0xffff0000, v70
	v_lshlrev_b32_e32 v66, 16, v67
	v_and_b32_e32 v67, 0xffff0000, v67
	v_pk_fma_f32 v[106:107], v[76:77], s[2:3], v[72:73] op_sel_hi:[1,0,1]
	v_pk_fma_f32 v[108:109], v[90:91], s[2:3], v[98:99] op_sel_hi:[1,0,1]
	v_pk_mul_f32 v[72:73], v[0:1], v[100:101]
	v_pk_mul_f32 v[74:75], v[2:3], v[74:75]
	v_pk_fma_f32 v[114:115], v[68:69], s[2:3], v[64:65] op_sel_hi:[1,0,1]
	v_pk_mul_f32 v[64:65], v[12:13], v[104:105]
	v_lshlrev_b32_e32 v70, 16, v71
	v_and_b32_e32 v71, 0xffff0000, v71
	v_pk_fma_f32 v[110:111], v[78:79], s[2:3], v[74:75] op_sel_hi:[1,0,1]
	v_pk_fma_f32 v[112:113], v[92:93], s[2:3], v[72:73] op_sel_hi:[1,0,1]
	v_pk_mul_f32 v[66:67], v[14:15], v[66:67]
	v_pk_fma_f32 v[120:121], v[96:97], s[2:3], v[64:65] op_sel_hi:[1,0,1]
	v_add_f32_e32 v64, v108, v109
	v_add_f32_e32 v65, v106, v107
	v_pk_mul_f32 v[72:73], v[4:5], v[102:103]
	v_pk_fma_f32 v[118:119], v[70:71], s[2:3], v[66:67] op_sel_hi:[1,0,1]
	v_add_f32_e32 v64, v64, v65
	v_add_f32_e32 v65, v112, v113
	v_add_f32_e32 v66, v110, v111
	v_pk_fma_f32 v[116:117], v[94:95], s[2:3], v[72:73] op_sel_hi:[1,0,1]
	v_add_f32_e32 v64, 0, v64
	v_add_f32_e32 v65, v65, v66
	v_add_f32_e32 v64, v65, v64
	v_add_f32_e32 v65, v116, v117
	v_add_f32_e32 v66, v114, v115
	v_add_f32_e32 v65, v65, v66
	v_add_f32_e32 v64, v65, v64
	v_add_f32_e32 v65, v120, v121
	v_add_f32_e32 v66, v118, v119
	v_add_f32_e32 v65, v65, v66
	v_add_f32_e32 v64, v65, v64
	s_nop 1
	v_mov_b32_dpp v65, v64 quad_perm:[1,0,3,2] row_mask:0xf bank_mask:0xf
	s_mov_b32 s2, 0x3727c5ac
	s_ashr_i32 s97, s96, 31
	s_lshl_b64 s[88:89], s[96:97], 11
	s_mov_b32 s33, 0xc0c0400
	s_waitcnt lgkmcnt(0)
	v_add_f32_e32 v64, v64, v65
	s_nop 1
	v_mov_b32_dpp v65, v64 quad_perm:[2,3,0,1] row_mask:0xf bank_mask:0xf
	s_lshl_b64 s[84:85], s[96:97], 10
	s_waitcnt lgkmcnt(0)
	v_add_f32_e32 v64, v64, v65
	s_nop 1
	v_mov_b32_dpp v65, v64 row_half_mirror row_mask:0xf bank_mask:0xf
	s_nop 1
	v_mov_b32_dpp v65, v65 quad_perm:[3,2,1,0] row_mask:0xf bank_mask:0xf
	s_waitcnt lgkmcnt(0)
	v_add_f32_e32 v64, v64, v65
	s_nop 1
	v_mov_b32_dpp v65, v64 row_ror:8 row_mask:0xf bank_mask:0xf
	s_waitcnt lgkmcnt(0)
	v_add_f32_e32 v64, v64, v65
	ds_swizzle_b32 v65, v64 offset:swizzle(SWAP,16)
	s_waitcnt lgkmcnt(0)
	v_add_f32_e32 v64, v64, v65
	v_mov_b32_e32 v65, v64
	s_nop 1
	v_permlane32_swap_b32_e32 v64, v65
	v_add_f32_e32 v64, v64, v65
	v_fmac_f32_e32 v107, 0xba800000, v64
	v_fmac_f32_e32 v109, 0xba800000, v64
	v_fmamk_f32 v106, v64, 0xba800000, v106
	v_fmamk_f32 v108, v64, 0xba800000, v108
	v_mul_f32_e32 v65, v109, v109
	v_mul_f32_e32 v66, v107, v107
	v_fmac_f32_e32 v65, v108, v108
	v_fmac_f32_e32 v66, v106, v106
	v_fmac_f32_e32 v111, 0xba800000, v64
	v_fmac_f32_e32 v113, 0xba800000, v64
	v_add_f32_e32 v65, v65, v66
	v_fmamk_f32 v110, v64, 0xba800000, v110
	v_fmamk_f32 v112, v64, 0xba800000, v112
	v_mul_f32_e32 v66, v113, v113
	v_mul_f32_e32 v67, v111, v111
	v_fmac_f32_e32 v66, v112, v112
	v_fmac_f32_e32 v67, v110, v110
	v_add_f32_e32 v66, v66, v67
	v_fmac_f32_e32 v115, 0xba800000, v64
	v_fmac_f32_e32 v117, 0xba800000, v64
	v_add_f32_e32 v65, v65, v66
	v_fmamk_f32 v114, v64, 0xba800000, v114
	v_fmamk_f32 v116, v64, 0xba800000, v116
	v_mul_f32_e32 v66, v117, v117
	v_mul_f32_e32 v67, v115, v115
	v_fmac_f32_e32 v66, v116, v116
	v_fmac_f32_e32 v67, v114, v114
	v_add_f32_e32 v66, v66, v67
	v_fmac_f32_e32 v119, 0xba800000, v64
	v_fmac_f32_e32 v121, 0xba800000, v64
	v_add_f32_e32 v65, v66, v65
	v_fmamk_f32 v118, v64, 0xba800000, v118
	v_fmamk_f32 v120, v64, 0xba800000, v120
	v_mul_f32_e32 v64, v121, v121
	v_mul_f32_e32 v66, v119, v119
	v_fmac_f32_e32 v64, v120, v120
	v_fmac_f32_e32 v66, v118, v118
	v_add_f32_e32 v64, v64, v66
	v_add_f32_e32 v64, v64, v65
	s_nop 1
	v_mov_b32_dpp v65, v64 quad_perm:[1,0,3,2] row_mask:0xf bank_mask:0xf
	s_waitcnt lgkmcnt(0)
	v_add_f32_e32 v64, v64, v65
	s_nop 1
	v_mov_b32_dpp v65, v64 quad_perm:[2,3,0,1] row_mask:0xf bank_mask:0xf
	s_waitcnt lgkmcnt(0)
	v_add_f32_e32 v64, v64, v65
	s_nop 1
	v_mov_b32_dpp v65, v64 row_half_mirror row_mask:0xf bank_mask:0xf
	s_nop 1
	v_mov_b32_dpp v65, v65 quad_perm:[3,2,1,0] row_mask:0xf bank_mask:0xf
	s_waitcnt lgkmcnt(0)
	v_add_f32_e32 v90, v64, v65
	s_nop 1
	v_mov_b32_dpp v91, v90 row_ror:8 row_mask:0xf bank_mask:0xf
	ds_read_b128 v[64:67], v123
	ds_read_b128 v[68:71], v123 offset:1024
	ds_read_b128 v[72:75], v124
	ds_read_b128 v[76:79], v124 offset:1024
	s_waitcnt lgkmcnt(4)
	v_add_f32_e32 v175, v90, v91
	ds_swizzle_b32 v176, v175 offset:swizzle(SWAP,16)
	ds_read_b128 v[90:93], v123 offset:2048
	ds_read_b128 v[94:97], v123 offset:3072
	ds_read_b128 v[98:101], v124 offset:2048
	ds_read_b128 v[102:105], v124 offset:3072
	s_waitcnt lgkmcnt(4)
	v_add_f32_e32 v175, v175, v176
	v_mov_b32_e32 v176, v175
	s_nop 1
	v_permlane32_swap_b32_e32 v175, v176
	v_add_f32_e32 v175, v175, v176
	v_mov_b32_e32 v176, s2
	v_fmac_f32_e32 v176, 0x3a800000, v175
	s_mov_b32 s2, 0x800000
	v_mul_f32_e32 v175, 0x4b800000, v176
	v_cmp_gt_f32_e32 vcc, s2, v176
	s_mov_b32 s2, 0x4b400000
	s_nop 0
	v_cndmask_b32_e32 v175, v176, v175, vcc
	v_rsq_f32_e32 v175, v175
	s_nop 0
	v_mul_f32_e32 v176, 0x45800000, v175
	v_cndmask_b32_e32 v176, v175, v176, vcc
	v_pk_mul_f32 v[108:109], v[108:109], v[176:177] op_sel_hi:[1,0]
	v_pk_mul_f32 v[106:107], v[106:107], v[176:177] op_sel_hi:[1,0]
	v_pk_fma_f32 v[64:65], v[64:65], v[108:109], v[72:73]
	v_pk_fma_f32 v[66:67], v[66:67], v[106:107], v[74:75]
	v_pk_mul_f32 v[72:73], v[112:113], v[176:177] op_sel_hi:[1,0]
	v_pk_mul_f32 v[74:75], v[110:111], v[176:177] op_sel_hi:[1,0]
	v_pk_fma_f32 v[68:69], v[68:69], v[72:73], v[76:77]
	v_pk_fma_f32 v[70:71], v[70:71], v[74:75], v[78:79]
	v_pk_mul_f32 v[72:73], v[116:117], v[176:177] op_sel_hi:[1,0]
	v_pk_mul_f32 v[76:77], v[120:121], v[176:177] op_sel_hi:[1,0]
	v_pk_mul_f32 v[74:75], v[114:115], v[176:177] op_sel_hi:[1,0]
	s_waitcnt lgkmcnt(1)
	v_pk_fma_f32 v[72:73], v[90:91], v[72:73], v[98:99]
	v_pk_mul_f32 v[78:79], v[118:119], v[176:177] op_sel_hi:[1,0]
	s_waitcnt lgkmcnt(0)
	v_pk_fma_f32 v[76:77], v[94:95], v[76:77], v[102:103]
	s_waitcnt vmcnt(0)
	v_pk_fma_f32 v[102:103], v[10:11], v[66:67], v[30:31]
	v_pk_fma_f32 v[98:99], v[38:39], v[70:71], v[18:19]
	v_pk_fma_f32 v[74:75], v[92:93], v[74:75], v[100:101]
	v_pk_fma_f32 v[78:79], v[96:97], v[78:79], v[104:105]
	v_pk_fma_f32 v[104:105], v[8:9], v[64:65], v[28:29]
	v_max_f32_e64 v90, |v102|, |v103|
	v_pk_fma_f32 v[100:101], v[36:37], v[68:69], v[16:17]
	v_max_f32_e64 v91, |v98|, |v99|
	v_max3_f32 v90, |v104|, |v105|, v90
	v_max3_f32 v91, |v100|, |v101|, v91
	v_pk_fma_f32 v[94:95], v[42:43], v[74:75], v[22:23]
	v_max3_f32 v106, v90, 0, v91
	v_pk_fma_f32 v[96:97], v[40:41], v[72:73], v[20:21]
	v_max_f32_e64 v90, |v94|, |v95|
	v_max3_f32 v107, |v96|, |v97|, v90
	v_pk_fma_f32 v[90:91], v[46:47], v[78:79], v[26:27]
	v_pk_fma_f32 v[92:93], v[44:45], v[76:77], v[24:25]
	v_max_f32_e64 v108, |v90|, |v91|
	v_max3_f32 v108, |v92|, |v93|, v108
	v_max3_f32 v106, v106, v107, v108
	s_nop 1
	v_mov_b32_dpp v107, v106 quad_perm:[1,0,3,2] row_mask:0xf bank_mask:0xf
	v_cvt_pk_bf16_f32 v64, v64, v65
	s_waitcnt lgkmcnt(0)
	v_max_f32_e32 v107, v107, v107
	v_max_f32_e32 v106, v106, v107
	s_nop 1
	v_mov_b32_dpp v107, v106 quad_perm:[2,3,0,1] row_mask:0xf bank_mask:0xf
	s_waitcnt lgkmcnt(0)
	v_max_f32_e32 v107, v107, v107
	v_max_f32_e32 v106, v106, v107
	s_nop 1
	v_mov_b32_dpp v107, v106 row_half_mirror row_mask:0xf bank_mask:0xf
	s_nop 1
	v_mov_b32_dpp v107, v107 quad_perm:[3,2,1,0] row_mask:0xf bank_mask:0xf
	s_waitcnt lgkmcnt(0)
	v_max_f32_e32 v65, v107, v107
	v_max_f32_e32 v106, v106, v65
	s_nop 1
	v_mov_b32_dpp v107, v106 row_ror:8 row_mask:0xf bank_mask:0xf
	v_cvt_pk_bf16_f32 v65, v66, v67
	v_cvt_pk_bf16_f32 v66, v68, v69
	v_cvt_pk_bf16_f32 v67, v70, v71
	v_lshl_add_u64 v[70:71], v[86:87], 0, s[88:89]
	s_waitcnt lgkmcnt(0)
	v_max_f32_e32 v68, v107, v107
	v_max_f32_e32 v68, v106, v68
	ds_swizzle_b32 v69, v68 offset:swizzle(SWAP,16)
	global_store_dwordx4 v[70:71], v[64:67], off
	s_nop 1
	v_cvt_pk_bf16_f32 v66, v72, v73
	s_waitcnt lgkmcnt(0)
	v_max_f32_e32 v64, v69, v69
	v_max_f32_e32 v64, v68, v64
	v_mov_b32_e32 v65, v64
	s_nop 1
	v_permlane32_swap_b32_e32 v64, v65
	v_max_f32_e32 v65, v65, v65
	v_max_f32_e32 v64, v64, v64
	v_max_f32_e32 v64, v64, v65
	v_mul_f32_e32 v65, 0x3c010204, v64
	v_cmp_lt_f32_e32 vcc, 0, v64
	v_cvt_pk_bf16_f32 v67, v74, v75
	v_cvt_pk_bf16_f32 v68, v76, v77
	v_cvt_pk_bf16_f32 v69, v78, v79
	global_store_dwordx4 v[70:71], v[66:69], off offset:16
	s_nop 0
	v_cndmask_b32_e32 v64, 1.0, v65, vcc
	v_div_scale_f32 v65, s[88:89], v64, v64, 1.0
	v_rcp_f32_e32 v72, v65
	s_mov_b32 s88, 0x4000c0c
	v_fma_f32 v66, -v65, v72, 1.0
	v_fmac_f32_e32 v72, v66, v72
	v_div_scale_f32 v66, vcc, 1.0, v64, 1.0
	v_mul_f32_e32 v67, v66, v72
	v_fma_f32 v68, -v65, v67, v66
	v_fmac_f32_e32 v67, v68, v72
	v_fma_f32 v65, -v65, v67, v66
	v_div_fmas_f32 v65, v65, v72, v67
	v_div_fixup_f32 v65, v65, v64, 1.0
	v_fma_f32 v66, v104, v65, s2
	v_fma_f32 v67, v105, v65, s2
	v_fma_f32 v68, v102, v65, s2
	v_fma_f32 v69, v103, v65, s2
	v_perm_b32 v66, v67, v66, s33
	v_perm_b32 v67, v69, v68, s88
	s_mov_b32 s2, 0x4b400000
	v_or_b32_e32 v66, v66, v67
	s_nop 0
	v_fma_f32 v67, v100, v65, s2
	v_fma_f32 v68, v101, v65, s2
	v_fma_f32 v69, v98, v65, s2
	v_fma_f32 v70, v99, v65, s2
	v_perm_b32 v67, v68, v67, s33
	v_perm_b32 v68, v70, v69, s88
	s_mov_b32 s2, 0x4b400000
	v_or_b32_e32 v67, v67, v68
	s_nop 0
	v_fma_f32 v68, v96, v65, s2
	v_fma_f32 v69, v97, v65, s2
	v_fma_f32 v70, v94, v65, s2
	v_fma_f32 v71, v95, v65, s2
	v_perm_b32 v68, v69, v68, s33
	v_perm_b32 v69, v71, v70, s88
	s_mov_b32 s2, 0x4b400000
	v_or_b32_e32 v68, v68, v69
	s_nop 0
	v_fma_f32 v69, v92, v65, s2
	v_fma_f32 v70, v93, v65, s2
	v_fma_f32 v71, v90, v65, s2
	v_fma_f32 v65, v91, v65, s2
	v_perm_b32 v69, v70, v69, s33
	v_perm_b32 v65, v65, v71, s88
	v_or_b32_e32 v69, v69, v65
	v_lshl_add_u64 v[70:71], v[88:89], 0, s[84:85]
	global_store_dwordx4 v[70:71], v[66:69], off
	s_and_saveexec_b64 s[84:85], s[6:7]
	s_cbranch_execz .LBB0_765
	s_lshl_b64 s[88:89], s[96:97], 2
	v_readlane_b32 s2, v254, 53
	s_add_u32 s88, s2, s88
	v_readlane_b32 s2, v254, 54
	s_addc_u32 s89, s2, s89
	global_store_dword v201, v64, s[88:89]
.LBB0_765:
	s_or_b64 exec, exec, s[84:85]
	v_lshlrev_b32_e32 v72, 16, v56
	v_and_b32_e32 v73, 0xffff0000, v56
	v_lshlrev_b32_e32 v56, 16, v57
	v_and_b32_e32 v57, 0xffff0000, v57
	v_lshlrev_b32_e32 v76, 16, v48
	v_and_b32_e32 v77, 0xffff0000, v48
	v_lshlrev_b32_e32 v48, 16, v49
	v_and_b32_e32 v49, 0xffff0000, v49
	v_lshlrev_b32_e32 v64, 16, v60
	v_and_b32_e32 v65, 0xffff0000, v60
	v_lshlrev_b32_e32 v60, 16, v61
	v_and_b32_e32 v61, 0xffff0000, v61
	v_lshlrev_b32_e32 v68, 16, v52
	v_and_b32_e32 v69, 0xffff0000, v52
	v_lshlrev_b32_e32 v52, 16, v53
	v_and_b32_e32 v53, 0xffff0000, v53
	v_lshlrev_b32_e32 v74, 16, v58
	v_and_b32_e32 v75, 0xffff0000, v58
	v_lshlrev_b32_e32 v58, 16, v59
	v_and_b32_e32 v59, 0xffff0000, v59
	v_lshlrev_b32_e32 v78, 16, v50
	v_and_b32_e32 v79, 0xffff0000, v50
	v_pk_mul_f32 v[72:73], v[32:33], v[72:73]
	v_pk_mul_f32 v[56:57], v[34:35], v[56:57]
	s_mov_b32 s2, 0x3fd744fd
	v_pk_mul_f32 v[48:49], v[6:7], v[48:49]
	v_lshlrev_b32_e32 v66, 16, v62
	v_and_b32_e32 v67, 0xffff0000, v62
	v_lshlrev_b32_e32 v62, 16, v63
	v_and_b32_e32 v63, 0xffff0000, v63
	v_lshlrev_b32_e32 v70, 16, v54
	v_and_b32_e32 v71, 0xffff0000, v54
	v_lshlrev_b32_e32 v50, 16, v51
	v_and_b32_e32 v51, 0xffff0000, v51
	v_pk_fma_f32 v[106:107], v[60:61], s[2:3], v[56:57] op_sel_hi:[1,0,1]
	v_pk_fma_f32 v[108:109], v[64:65], s[2:3], v[72:73] op_sel_hi:[1,0,1]
	v_pk_mul_f32 v[56:57], v[0:1], v[74:75]
	v_pk_mul_f32 v[58:59], v[2:3], v[58:59]
	v_pk_fma_f32 v[114:115], v[52:53], s[2:3], v[48:49] op_sel_hi:[1,0,1]
	v_pk_mul_f32 v[48:49], v[12:13], v[78:79]
	v_lshlrev_b32_e32 v54, 16, v55
	v_and_b32_e32 v55, 0xffff0000, v55
	v_pk_fma_f32 v[110:111], v[62:63], s[2:3], v[58:59] op_sel_hi:[1,0,1]
	v_pk_fma_f32 v[112:113], v[66:67], s[2:3], v[56:57] op_sel_hi:[1,0,1]
	v_pk_mul_f32 v[50:51], v[14:15], v[50:51]
	v_pk_fma_f32 v[120:121], v[70:71], s[2:3], v[48:49] op_sel_hi:[1,0,1]
	v_add_f32_e32 v48, v108, v109
	v_add_f32_e32 v49, v106, v107
	v_pk_mul_f32 v[56:57], v[4:5], v[76:77]
	v_pk_fma_f32 v[118:119], v[54:55], s[2:3], v[50:51] op_sel_hi:[1,0,1]
	v_add_f32_e32 v48, v48, v49
	v_add_f32_e32 v49, v112, v113
	v_add_f32_e32 v50, v110, v111
	v_pk_fma_f32 v[116:117], v[68:69], s[2:3], v[56:57] op_sel_hi:[1,0,1]
	v_add_f32_e32 v48, 0, v48
	v_add_f32_e32 v49, v49, v50
	v_add_f32_e32 v48, v49, v48
	v_add_f32_e32 v49, v116, v117
	v_add_f32_e32 v50, v114, v115
	v_add_f32_e32 v49, v49, v50
	v_add_f32_e32 v48, v49, v48
	v_add_f32_e32 v49, v120, v121
	v_add_f32_e32 v50, v118, v119
	v_add_f32_e32 v49, v49, v50
	v_add_f32_e32 v48, v49, v48
	s_nop 1
	v_mov_b32_dpp v49, v48 quad_perm:[1,0,3,2] row_mask:0xf bank_mask:0xf
	s_mov_b32 s2, 0x3727c5ac
	s_add_i32 s94, s96, 1
	s_ashr_i32 s95, s94, 31
	s_lshl_b64 s[88:89], s[94:95], 11
	s_waitcnt lgkmcnt(0)
	v_add_f32_e32 v48, v48, v49
	s_nop 1
	v_mov_b32_dpp v49, v48 quad_perm:[2,3,0,1] row_mask:0xf bank_mask:0xf
	s_lshl_b64 s[84:85], s[94:95], 10
	s_waitcnt lgkmcnt(0)
	v_add_f32_e32 v48, v48, v49
	s_nop 1
	v_mov_b32_dpp v49, v48 row_half_mirror row_mask:0xf bank_mask:0xf
	s_nop 1
	v_mov_b32_dpp v49, v49 quad_perm:[3,2,1,0] row_mask:0xf bank_mask:0xf
	s_waitcnt lgkmcnt(0)
	v_add_f32_e32 v48, v48, v49
	s_nop 1
	v_mov_b32_dpp v49, v48 row_ror:8 row_mask:0xf bank_mask:0xf
	s_waitcnt lgkmcnt(0)
	v_add_f32_e32 v48, v48, v49
	ds_swizzle_b32 v49, v48 offset:swizzle(SWAP,16)
	s_waitcnt lgkmcnt(0)
	v_add_f32_e32 v48, v48, v49
	v_mov_b32_e32 v49, v48
	s_nop 1
	v_permlane32_swap_b32_e32 v48, v49
	v_add_f32_e32 v48, v48, v49
	v_fmac_f32_e32 v107, 0xba800000, v48
	v_fmac_f32_e32 v109, 0xba800000, v48
	v_fmamk_f32 v106, v48, 0xba800000, v106
	v_fmamk_f32 v108, v48, 0xba800000, v108
	v_mul_f32_e32 v49, v109, v109
	v_mul_f32_e32 v50, v107, v107
	v_fmac_f32_e32 v49, v108, v108
	v_fmac_f32_e32 v50, v106, v106
	v_fmac_f32_e32 v111, 0xba800000, v48
	v_fmac_f32_e32 v113, 0xba800000, v48
	v_add_f32_e32 v49, v49, v50
	v_fmamk_f32 v110, v48, 0xba800000, v110
	v_fmamk_f32 v112, v48, 0xba800000, v112
	v_mul_f32_e32 v50, v113, v113
	v_mul_f32_e32 v51, v111, v111
	v_fmac_f32_e32 v50, v112, v112
	v_fmac_f32_e32 v51, v110, v110
	v_add_f32_e32 v50, v50, v51
	v_fmac_f32_e32 v115, 0xba800000, v48
	v_fmac_f32_e32 v117, 0xba800000, v48
	v_add_f32_e32 v49, v49, v50
	v_fmamk_f32 v114, v48, 0xba800000, v114
	v_fmamk_f32 v116, v48, 0xba800000, v116
	v_mul_f32_e32 v50, v117, v117
	v_mul_f32_e32 v51, v115, v115
	v_fmac_f32_e32 v50, v116, v116
	v_fmac_f32_e32 v51, v114, v114
	v_add_f32_e32 v50, v50, v51
	v_fmac_f32_e32 v119, 0xba800000, v48
	v_fmac_f32_e32 v121, 0xba800000, v48
	v_add_f32_e32 v49, v50, v49
	v_fmamk_f32 v118, v48, 0xba800000, v118
	v_fmamk_f32 v120, v48, 0xba800000, v120
	v_mul_f32_e32 v48, v121, v121
	v_mul_f32_e32 v50, v119, v119
	v_fmac_f32_e32 v48, v120, v120
	v_fmac_f32_e32 v50, v118, v118
	v_add_f32_e32 v48, v48, v50
	v_add_f32_e32 v48, v48, v49
	s_nop 1
	v_mov_b32_dpp v49, v48 quad_perm:[1,0,3,2] row_mask:0xf bank_mask:0xf
	s_waitcnt lgkmcnt(0)
	v_add_f32_e32 v48, v48, v49
	s_nop 1
	v_mov_b32_dpp v49, v48 quad_perm:[2,3,0,1] row_mask:0xf bank_mask:0xf
	s_waitcnt lgkmcnt(0)
	v_add_f32_e32 v48, v48, v49
	s_nop 1
	v_mov_b32_dpp v49, v48 row_half_mirror row_mask:0xf bank_mask:0xf
	s_nop 1
	v_mov_b32_dpp v49, v49 quad_perm:[3,2,1,0] row_mask:0xf bank_mask:0xf
	s_waitcnt lgkmcnt(0)
	v_add_f32_e32 v64, v48, v49
	s_nop 1
	v_mov_b32_dpp v65, v64 row_ror:8 row_mask:0xf bank_mask:0xf
	ds_read_b128 v[48:51], v123
	ds_read_b128 v[52:55], v123 offset:1024
	ds_read_b128 v[56:59], v124
	ds_read_b128 v[60:63], v124 offset:1024
	s_waitcnt lgkmcnt(4)
	v_add_f32_e32 v175, v64, v65
	ds_swizzle_b32 v176, v175 offset:swizzle(SWAP,16)
	ds_read_b128 v[64:67], v123 offset:2048
	ds_read_b128 v[68:71], v123 offset:3072
	ds_read_b128 v[72:75], v124 offset:2048
	ds_read_b128 v[76:79], v124 offset:3072
	s_waitcnt lgkmcnt(4)
	v_add_f32_e32 v175, v175, v176
	v_mov_b32_e32 v176, v175
	s_nop 1
	v_permlane32_swap_b32_e32 v175, v176
	v_add_f32_e32 v175, v175, v176
	v_mov_b32_e32 v176, s2
	v_fmac_f32_e32 v176, 0x3a800000, v175
	s_mov_b32 s2, 0x800000
	v_mul_f32_e32 v175, 0x4b800000, v176
	v_cmp_gt_f32_e32 vcc, s2, v176
	s_mov_b32 s2, 0x4b400000
	s_nop 0
	v_cndmask_b32_e32 v175, v176, v175, vcc
	v_rsq_f32_e32 v175, v175
	s_nop 0
	v_mul_f32_e32 v176, 0x45800000, v175
	v_cndmask_b32_e32 v176, v175, v176, vcc
	v_pk_mul_f32 v[106:107], v[106:107], v[176:177] op_sel_hi:[1,0]
	v_pk_mul_f32 v[108:109], v[108:109], v[176:177] op_sel_hi:[1,0]
	v_pk_fma_f32 v[50:51], v[50:51], v[106:107], v[58:59]
	v_pk_mul_f32 v[58:59], v[110:111], v[176:177] op_sel_hi:[1,0]
	v_pk_fma_f32 v[48:49], v[48:49], v[108:109], v[56:57]
	v_pk_mul_f32 v[56:57], v[112:113], v[176:177] op_sel_hi:[1,0]
	v_pk_fma_f32 v[54:55], v[54:55], v[58:59], v[62:63]
	v_pk_fma_f32 v[52:53], v[52:53], v[56:57], v[60:61]
	v_pk_mul_f32 v[56:57], v[116:117], v[176:177] op_sel_hi:[1,0]
	v_pk_mul_f32 v[58:59], v[114:115], v[176:177] op_sel_hi:[1,0]
	v_pk_mul_f32 v[62:63], v[118:119], v[176:177] op_sel_hi:[1,0]
	v_pk_fma_f32 v[118:119], v[10:11], v[50:51], v[30:31]
	v_pk_fma_f32 v[114:115], v[38:39], v[54:55], v[18:19]
	s_waitcnt lgkmcnt(1)
	v_pk_fma_f32 v[58:59], v[66:67], v[58:59], v[74:75]
	v_pk_fma_f32 v[56:57], v[64:65], v[56:57], v[72:73]
	v_pk_mul_f32 v[60:61], v[120:121], v[176:177] op_sel_hi:[1,0]
	s_waitcnt lgkmcnt(0)
	v_pk_fma_f32 v[62:63], v[70:71], v[62:63], v[78:79]
	v_pk_fma_f32 v[120:121], v[8:9], v[48:49], v[28:29]
	v_max_f32_e64 v64, |v118|, |v119|
	v_pk_fma_f32 v[116:117], v[36:37], v[52:53], v[16:17]
	v_max_f32_e64 v65, |v114|, |v115|
	v_pk_fma_f32 v[60:61], v[68:69], v[60:61], v[76:77]
	v_max3_f32 v64, |v120|, |v121|, v64
	v_max3_f32 v65, |v116|, |v117|, v65
	v_pk_fma_f32 v[110:111], v[42:43], v[58:59], v[22:23]
	v_pk_fma_f32 v[106:107], v[46:47], v[62:63], v[26:27]
	v_max3_f32 v64, v64, 0, v65
	v_pk_fma_f32 v[112:113], v[40:41], v[56:57], v[20:21]
	v_max_f32_e64 v65, |v110|, |v111|
	v_pk_fma_f32 v[108:109], v[44:45], v[60:61], v[24:25]
	v_max_f32_e64 v66, |v106|, |v107|
	v_max3_f32 v65, |v112|, |v113|, v65
	v_max3_f32 v66, |v108|, |v109|, v66
	v_max3_f32 v64, v64, v65, v66
	s_nop 1
	v_mov_b32_dpp v65, v64 quad_perm:[1,0,3,2] row_mask:0xf bank_mask:0xf
	v_cvt_pk_bf16_f32 v48, v48, v49
	s_waitcnt lgkmcnt(0)
	v_max_f32_e32 v65, v65, v65
	v_max_f32_e32 v64, v64, v65
	s_nop 1
	v_mov_b32_dpp v65, v64 quad_perm:[2,3,0,1] row_mask:0xf bank_mask:0xf
	s_waitcnt lgkmcnt(0)
	v_max_f32_e32 v65, v65, v65
	v_max_f32_e32 v64, v64, v65
	s_nop 1
	v_mov_b32_dpp v65, v64 row_half_mirror row_mask:0xf bank_mask:0xf
	s_nop 1
	v_mov_b32_dpp v65, v65 quad_perm:[3,2,1,0] row_mask:0xf bank_mask:0xf
	s_waitcnt lgkmcnt(0)
	v_max_f32_e32 v49, v65, v65
	v_max_f32_e32 v64, v64, v49
	s_nop 1
	v_mov_b32_dpp v65, v64 row_ror:8 row_mask:0xf bank_mask:0xf
	v_cvt_pk_bf16_f32 v49, v50, v51
	v_cvt_pk_bf16_f32 v50, v52, v53
	v_cvt_pk_bf16_f32 v51, v54, v55
	v_lshl_add_u64 v[54:55], v[86:87], 0, s[88:89]
	s_waitcnt lgkmcnt(0)
	v_max_f32_e32 v52, v65, v65
	v_max_f32_e32 v52, v64, v52
	ds_swizzle_b32 v53, v52 offset:swizzle(SWAP,16)
	global_store_dwordx4 v[54:55], v[48:51], off
	s_nop 1
	v_cvt_pk_bf16_f32 v50, v56, v57
	s_waitcnt lgkmcnt(0)
	v_max_f32_e32 v48, v53, v53
	v_max_f32_e32 v48, v52, v48
	v_mov_b32_e32 v49, v48
	s_nop 1
	v_permlane32_swap_b32_e32 v48, v49
	v_max_f32_e32 v49, v49, v49
	v_max_f32_e32 v48, v48, v48
	v_max_f32_e32 v48, v48, v49
	v_mul_f32_e32 v49, 0x3c010204, v48
	v_cmp_lt_f32_e32 vcc, 0, v48
	v_cvt_pk_bf16_f32 v51, v58, v59
	v_cvt_pk_bf16_f32 v52, v60, v61
	v_cvt_pk_bf16_f32 v53, v62, v63
	global_store_dwordx4 v[54:55], v[50:53], off offset:16
	s_nop 0
	v_cndmask_b32_e32 v48, 1.0, v49, vcc
	v_div_scale_f32 v49, s[88:89], v48, v48, 1.0
	v_rcp_f32_e32 v56, v49
	s_mov_b32 s88, 0x4000c0c
	v_fma_f32 v50, -v49, v56, 1.0
	v_fmac_f32_e32 v56, v50, v56
	v_div_scale_f32 v50, vcc, 1.0, v48, 1.0
	v_mul_f32_e32 v51, v50, v56
	v_fma_f32 v52, -v49, v51, v50
	v_fmac_f32_e32 v51, v52, v56
	v_fma_f32 v49, -v49, v51, v50
	v_div_fmas_f32 v49, v49, v56, v51
	v_div_fixup_f32 v49, v49, v48, 1.0
	v_fma_f32 v50, v120, v49, s2
	v_fma_f32 v51, v121, v49, s2
	v_fma_f32 v52, v118, v49, s2
	v_fma_f32 v53, v119, v49, s2
	v_perm_b32 v50, v51, v50, s33
	v_perm_b32 v51, v53, v52, s88
	s_mov_b32 s2, 0x4b400000
	v_or_b32_e32 v50, v50, v51
	s_nop 0
	v_fma_f32 v51, v116, v49, s2
	v_fma_f32 v52, v117, v49, s2
	v_fma_f32 v53, v114, v49, s2
	v_fma_f32 v54, v115, v49, s2
	v_perm_b32 v51, v52, v51, s33
	v_perm_b32 v52, v54, v53, s88
	s_mov_b32 s2, 0x4b400000
	v_or_b32_e32 v51, v51, v52
	s_nop 0
	v_fma_f32 v52, v112, v49, s2
	v_fma_f32 v53, v113, v49, s2
	v_fma_f32 v54, v110, v49, s2
	v_fma_f32 v55, v111, v49, s2
	v_perm_b32 v52, v53, v52, s33
	v_perm_b32 v53, v55, v54, s88
	s_mov_b32 s2, 0x4b400000
	v_or_b32_e32 v52, v52, v53
	s_nop 0
	v_fma_f32 v53, v108, v49, s2
	v_fma_f32 v54, v109, v49, s2
	v_fma_f32 v55, v106, v49, s2
	v_fma_f32 v49, v107, v49, s2
	v_perm_b32 v53, v54, v53, s33
	v_perm_b32 v49, v49, v55, s88
	v_or_b32_e32 v53, v53, v49
	v_lshl_add_u64 v[54:55], v[88:89], 0, s[84:85]
	global_store_dwordx4 v[54:55], v[50:53], off
	s_and_saveexec_b64 s[84:85], s[6:7]
	s_cbranch_execz .LBB0_767
	s_lshl_b64 s[88:89], s[94:95], 2
	v_readlane_b32 s2, v254, 53
	s_add_u32 s88, s2, s88
	v_readlane_b32 s2, v254, 54
	s_addc_u32 s89, s2, s89
	global_store_dword v201, v48, s[88:89]
.LBB0_767:
	s_or_b64 exec, exec, s[84:85]
	s_add_i32 s2, s3, 1
	s_cmp_ge_i32 s2, s90
	s_cselect_b64 s[88:89], -1, 0
	s_cmp_lt_i32 s2, s90
	s_cselect_b32 s3, s2, s3
	s_lshl_b32 s84, s3, 1
	s_ashr_i32 s85, s84, 31
	s_lshl_b64 s[92:93], s[84:85], 11
	s_or_b32 s84, s84, 1
	s_ashr_i32 s85, s84, 31
	v_lshl_add_u64 v[48:49], v[82:83], 0, s[92:93]
	s_lshl_b64 s[84:85], s[84:85], 11
	v_lshl_add_u64 v[50:51], v[84:85], 0, s[92:93]
	global_load_dwordx4 v[68:71], v[48:49], off offset:16
	global_load_dwordx4 v[76:79], v[48:49], off
	global_load_dwordx4 v[64:67], v[50:51], off offset:16
	global_load_dwordx4 v[72:75], v[50:51], off
	v_lshl_add_u64 v[48:49], v[82:83], 0, s[84:85]
	v_lshl_add_u64 v[56:57], v[84:85], 0, s[84:85]
	global_load_dwordx4 v[52:55], v[48:49], off offset:16
	global_load_dwordx4 v[60:63], v[48:49], off
	s_nop 0
	global_load_dwordx4 v[48:51], v[56:57], off offset:16
	s_nop 0
	global_load_dwordx4 v[56:59], v[56:57], off
	s_waitcnt lgkmcnt(0)
	ds_read_b128 v[130:133], v125
	ds_read_b128 v[134:137], v125 offset:1024
	ds_read_b128 v[138:141], v125 offset:2048
	ds_read_b128 v[142:145], v125 offset:3072
	ds_read_b128 v[146:149], v125 offset:4096
	ds_read_b128 v[150:153], v125 offset:5120
	ds_read_b128 v[154:157], v125 offset:6144
	ds_read_b128 v[158:161], v125 offset:7168
	s_waitcnt lgkmcnt(7)
	v_pk_fma_f32 v[162:163], v[104:105], v[130:131], 0 op_sel_hi:[1,1,0]
	v_pk_fma_f32 v[164:165], v[120:121], v[130:131], 0 op_sel_hi:[1,1,0]
	v_pk_fma_f32 v[162:163], v[102:103], v[132:133], v[162:163]
	v_pk_fma_f32 v[164:165], v[118:119], v[132:133], v[164:165]
	ds_read_b128 v[130:133], v125 offset:8192
	s_waitcnt lgkmcnt(7)
	v_pk_fma_f32 v[162:163], v[100:101], v[134:135], v[162:163]
	v_pk_fma_f32 v[164:165], v[116:117], v[134:135], v[164:165]
	v_pk_fma_f32 v[162:163], v[98:99], v[136:137], v[162:163]
	v_pk_fma_f32 v[164:165], v[114:115], v[136:137], v[164:165]
	ds_read_b128 v[134:137], v125 offset:9216
	s_waitcnt lgkmcnt(7)
	v_pk_fma_f32 v[162:163], v[96:97], v[138:139], v[162:163]
	v_pk_fma_f32 v[164:165], v[112:113], v[138:139], v[164:165]
	v_pk_fma_f32 v[162:163], v[94:95], v[140:141], v[162:163]
	v_pk_fma_f32 v[164:165], v[110:111], v[140:141], v[164:165]
	ds_read_b128 v[138:141], v125 offset:10240
	s_waitcnt lgkmcnt(7)
	v_pk_fma_f32 v[162:163], v[92:93], v[142:143], v[162:163]
	v_pk_fma_f32 v[164:165], v[108:109], v[142:143], v[164:165]
	v_pk_fma_f32 v[162:163], v[90:91], v[144:145], v[162:163]
	v_pk_fma_f32 v[164:165], v[106:107], v[144:145], v[164:165]
	v_add_f32_e32 v178, v162, v163
	v_add_f32_e32 v175, v164, v165
	ds_read_b128 v[142:145], v125 offset:11264
	s_waitcnt lgkmcnt(7)
	v_pk_fma_f32 v[162:163], v[104:105], v[146:147], 0 op_sel_hi:[1,1,0]
	v_pk_fma_f32 v[164:165], v[120:121], v[146:147], 0 op_sel_hi:[1,1,0]
	v_pk_fma_f32 v[162:163], v[102:103], v[148:149], v[162:163]
	v_pk_fma_f32 v[164:165], v[118:119], v[148:149], v[164:165]
	ds_read_b128 v[146:149], v125 offset:12288
	s_waitcnt lgkmcnt(7)
	v_pk_fma_f32 v[162:163], v[100:101], v[150:151], v[162:163]
	v_pk_fma_f32 v[164:165], v[116:117], v[150:151], v[164:165]
	v_pk_fma_f32 v[162:163], v[98:99], v[152:153], v[162:163]
	v_pk_fma_f32 v[164:165], v[114:115], v[152:153], v[164:165]
	ds_read_b128 v[150:153], v125 offset:13312
	s_waitcnt lgkmcnt(7)
	v_pk_fma_f32 v[162:163], v[96:97], v[154:155], v[162:163]
	v_pk_fma_f32 v[164:165], v[112:113], v[154:155], v[164:165]
	v_pk_fma_f32 v[162:163], v[94:95], v[156:157], v[162:163]
	v_pk_fma_f32 v[164:165], v[110:111], v[156:157], v[164:165]
	ds_read_b128 v[154:157], v125 offset:14336
	s_waitcnt lgkmcnt(7)
	v_pk_fma_f32 v[162:163], v[92:93], v[158:159], v[162:163]
	v_pk_fma_f32 v[164:165], v[108:109], v[158:159], v[164:165]
	v_pk_fma_f32 v[162:163], v[90:91], v[160:161], v[162:163]
	v_pk_fma_f32 v[164:165], v[106:107], v[160:161], v[164:165]
	v_add_f32_e32 v180, v162, v163
	v_add_f32_e32 v176, v164, v165
	ds_read_b128 v[158:161], v125 offset:15360
	s_waitcnt lgkmcnt(7)
	v_pk_fma_f32 v[162:163], v[104:105], v[130:131], 0 op_sel_hi:[1,1,0]
	v_pk_fma_f32 v[164:165], v[120:121], v[130:131], 0 op_sel_hi:[1,1,0]
	v_pk_fma_f32 v[162:163], v[102:103], v[132:133], v[162:163]
	v_pk_fma_f32 v[164:165], v[118:119], v[132:133], v[164:165]
	ds_read_b128 v[130:133], v125 offset:16384
	s_waitcnt lgkmcnt(7)
	v_pk_fma_f32 v[162:163], v[100:101], v[134:135], v[162:163]
	v_pk_fma_f32 v[164:165], v[116:117], v[134:135], v[164:165]
	v_pk_fma_f32 v[162:163], v[98:99], v[136:137], v[162:163]
	v_pk_fma_f32 v[164:165], v[114:115], v[136:137], v[164:165]
	ds_read_b128 v[134:137], v125 offset:17408
	s_waitcnt lgkmcnt(7)
	v_pk_fma_f32 v[162:163], v[96:97], v[138:139], v[162:163]
	v_pk_fma_f32 v[164:165], v[112:113], v[138:139], v[164:165]
	v_pk_fma_f32 v[162:163], v[94:95], v[140:141], v[162:163]
	v_pk_fma_f32 v[164:165], v[110:111], v[140:141], v[164:165]
	ds_read_b128 v[138:141], v125 offset:18432
	s_waitcnt lgkmcnt(7)
	v_pk_fma_f32 v[162:163], v[92:93], v[142:143], v[162:163]
	v_pk_fma_f32 v[164:165], v[108:109], v[142:143], v[164:165]
	v_pk_fma_f32 v[162:163], v[90:91], v[144:145], v[162:163]
	v_pk_fma_f32 v[164:165], v[106:107], v[144:145], v[164:165]
	v_add_f32_e32 v182, v162, v163
	v_add_f32_e32 v177, v164, v165
	ds_read_b128 v[142:145], v125 offset:19456
	s_waitcnt lgkmcnt(7)
	v_pk_fma_f32 v[162:163], v[104:105], v[146:147], 0 op_sel_hi:[1,1,0]
	v_pk_fma_f32 v[164:165], v[120:121], v[146:147], 0 op_sel_hi:[1,1,0]
	v_pk_fma_f32 v[162:163], v[102:103], v[148:149], v[162:163]
	v_pk_fma_f32 v[164:165], v[118:119], v[148:149], v[164:165]
	ds_read_b128 v[146:149], v125 offset:20480
	s_waitcnt lgkmcnt(7)
	v_pk_fma_f32 v[162:163], v[100:101], v[150:151], v[162:163]
	v_pk_fma_f32 v[164:165], v[116:117], v[150:151], v[164:165]
	v_pk_fma_f32 v[162:163], v[98:99], v[152:153], v[162:163]
	v_pk_fma_f32 v[164:165], v[114:115], v[152:153], v[164:165]
	ds_read_b128 v[150:153], v125 offset:21504
	s_waitcnt lgkmcnt(7)
	v_pk_fma_f32 v[162:163], v[96:97], v[154:155], v[162:163]
	v_pk_fma_f32 v[164:165], v[112:113], v[154:155], v[164:165]
	v_pk_fma_f32 v[162:163], v[94:95], v[156:157], v[162:163]
	v_pk_fma_f32 v[164:165], v[110:111], v[156:157], v[164:165]
	ds_read_b128 v[154:157], v125 offset:22528
	s_waitcnt lgkmcnt(7)
	v_pk_fma_f32 v[162:163], v[92:93], v[158:159], v[162:163]
	v_pk_fma_f32 v[164:165], v[108:109], v[158:159], v[164:165]
	v_pk_fma_f32 v[162:163], v[90:91], v[160:161], v[162:163]
	v_pk_fma_f32 v[164:165], v[106:107], v[160:161], v[164:165]
	v_add_f32_e32 v184, v162, v163
	v_add_f32_e32 v179, v164, v165
	ds_read_b128 v[158:161], v125 offset:23552
	s_waitcnt lgkmcnt(7)
	v_pk_fma_f32 v[162:163], v[104:105], v[130:131], 0 op_sel_hi:[1,1,0]
	v_pk_fma_f32 v[164:165], v[120:121], v[130:131], 0 op_sel_hi:[1,1,0]
	v_pk_fma_f32 v[162:163], v[102:103], v[132:133], v[162:163]
	v_pk_fma_f32 v[164:165], v[118:119], v[132:133], v[164:165]
	ds_read_b128 v[130:133], v125 offset:24576
	s_waitcnt lgkmcnt(7)
	v_pk_fma_f32 v[162:163], v[100:101], v[134:135], v[162:163]
	v_pk_fma_f32 v[164:165], v[116:117], v[134:135], v[164:165]
	v_pk_fma_f32 v[162:163], v[98:99], v[136:137], v[162:163]
	v_pk_fma_f32 v[164:165], v[114:115], v[136:137], v[164:165]
	ds_read_b128 v[134:137], v125 offset:25600
	s_waitcnt lgkmcnt(7)
	v_pk_fma_f32 v[162:163], v[96:97], v[138:139], v[162:163]
	v_pk_fma_f32 v[164:165], v[112:113], v[138:139], v[164:165]
	v_pk_fma_f32 v[162:163], v[94:95], v[140:141], v[162:163]
	v_pk_fma_f32 v[164:165], v[110:111], v[140:141], v[164:165]
	ds_read_b128 v[138:141], v125 offset:26624
	s_waitcnt lgkmcnt(7)
	v_pk_fma_f32 v[162:163], v[92:93], v[142:143], v[162:163]
	v_pk_fma_f32 v[164:165], v[108:109], v[142:143], v[164:165]
	v_pk_fma_f32 v[162:163], v[90:91], v[144:145], v[162:163]
	v_pk_fma_f32 v[164:165], v[106:107], v[144:145], v[164:165]
	v_add_f32_e32 v186, v162, v163
	v_add_f32_e32 v181, v164, v165
	ds_read_b128 v[142:145], v125 offset:27648
	s_waitcnt lgkmcnt(7)
	v_pk_fma_f32 v[162:163], v[104:105], v[146:147], 0 op_sel_hi:[1,1,0]
	v_pk_fma_f32 v[164:165], v[120:121], v[146:147], 0 op_sel_hi:[1,1,0]
	v_pk_fma_f32 v[162:163], v[102:103], v[148:149], v[162:163]
	v_pk_fma_f32 v[164:165], v[118:119], v[148:149], v[164:165]
	ds_read_b128 v[146:149], v125 offset:28672
	s_waitcnt lgkmcnt(7)
	v_pk_fma_f32 v[162:163], v[100:101], v[150:151], v[162:163]
	v_pk_fma_f32 v[164:165], v[116:117], v[150:151], v[164:165]
	v_pk_fma_f32 v[162:163], v[98:99], v[152:153], v[162:163]
	v_pk_fma_f32 v[164:165], v[114:115], v[152:153], v[164:165]
	ds_read_b128 v[150:153], v125 offset:29696
	s_waitcnt lgkmcnt(7)
	v_pk_fma_f32 v[162:163], v[96:97], v[154:155], v[162:163]
	v_pk_fma_f32 v[164:165], v[112:113], v[154:155], v[164:165]
	v_pk_fma_f32 v[162:163], v[94:95], v[156:157], v[162:163]
	v_pk_fma_f32 v[164:165], v[110:111], v[156:157], v[164:165]
	ds_read_b128 v[154:157], v125 offset:30720
	s_waitcnt lgkmcnt(7)
	v_pk_fma_f32 v[162:163], v[92:93], v[158:159], v[162:163]
	v_pk_fma_f32 v[164:165], v[108:109], v[158:159], v[164:165]
	v_pk_fma_f32 v[162:163], v[90:91], v[160:161], v[162:163]
	v_pk_fma_f32 v[164:165], v[106:107], v[160:161], v[164:165]
	v_add_f32_e32 v188, v162, v163
	v_add_f32_e32 v183, v164, v165
	ds_read_b128 v[158:161], v125 offset:31744
	s_waitcnt lgkmcnt(7)
	v_pk_fma_f32 v[162:163], v[104:105], v[130:131], 0 op_sel_hi:[1,1,0]
	v_pk_fma_f32 v[164:165], v[120:121], v[130:131], 0 op_sel_hi:[1,1,0]
	v_pk_fma_f32 v[162:163], v[102:103], v[132:133], v[162:163]
	v_pk_fma_f32 v[164:165], v[118:119], v[132:133], v[164:165]
	ds_read_b128 v[130:133], v125 offset:32768
	s_waitcnt lgkmcnt(7)
	v_pk_fma_f32 v[162:163], v[100:101], v[134:135], v[162:163]
	v_pk_fma_f32 v[164:165], v[116:117], v[134:135], v[164:165]
	v_pk_fma_f32 v[162:163], v[98:99], v[136:137], v[162:163]
	v_pk_fma_f32 v[164:165], v[114:115], v[136:137], v[164:165]
	ds_read_b128 v[134:137], v125 offset:33792
	s_waitcnt lgkmcnt(7)
	v_pk_fma_f32 v[162:163], v[96:97], v[138:139], v[162:163]
	v_pk_fma_f32 v[164:165], v[112:113], v[138:139], v[164:165]
	v_pk_fma_f32 v[162:163], v[94:95], v[140:141], v[162:163]
	v_pk_fma_f32 v[164:165], v[110:111], v[140:141], v[164:165]
	ds_read_b128 v[138:141], v125 offset:34816
	s_waitcnt lgkmcnt(7)
	v_pk_fma_f32 v[162:163], v[92:93], v[142:143], v[162:163]
	v_pk_fma_f32 v[164:165], v[108:109], v[142:143], v[164:165]
	v_pk_fma_f32 v[162:163], v[90:91], v[144:145], v[162:163]
	v_pk_fma_f32 v[164:165], v[106:107], v[144:145], v[164:165]
	v_add_f32_e32 v190, v162, v163
	v_add_f32_e32 v185, v164, v165
	ds_read_b128 v[142:145], v125 offset:35840
	s_waitcnt lgkmcnt(7)
	v_pk_fma_f32 v[162:163], v[104:105], v[146:147], 0 op_sel_hi:[1,1,0]
	v_pk_fma_f32 v[164:165], v[120:121], v[146:147], 0 op_sel_hi:[1,1,0]
	v_pk_fma_f32 v[162:163], v[102:103], v[148:149], v[162:163]
	v_pk_fma_f32 v[164:165], v[118:119], v[148:149], v[164:165]
	ds_read_b128 v[146:149], v125 offset:36864
	s_waitcnt lgkmcnt(7)
	v_pk_fma_f32 v[162:163], v[100:101], v[150:151], v[162:163]
	v_pk_fma_f32 v[164:165], v[116:117], v[150:151], v[164:165]
	v_pk_fma_f32 v[162:163], v[98:99], v[152:153], v[162:163]
	v_pk_fma_f32 v[164:165], v[114:115], v[152:153], v[164:165]
	ds_read_b128 v[150:153], v125 offset:37888
	s_waitcnt lgkmcnt(7)
	v_pk_fma_f32 v[162:163], v[96:97], v[154:155], v[162:163]
	v_pk_fma_f32 v[164:165], v[112:113], v[154:155], v[164:165]
	v_pk_fma_f32 v[162:163], v[94:95], v[156:157], v[162:163]
	v_pk_fma_f32 v[164:165], v[110:111], v[156:157], v[164:165]
	ds_read_b128 v[154:157], v125 offset:38912
	s_waitcnt lgkmcnt(7)
	v_pk_fma_f32 v[162:163], v[92:93], v[158:159], v[162:163]
	v_pk_fma_f32 v[164:165], v[108:109], v[158:159], v[164:165]
	v_pk_fma_f32 v[162:163], v[90:91], v[160:161], v[162:163]
	v_pk_fma_f32 v[164:165], v[106:107], v[160:161], v[164:165]
	v_add_f32_e32 v192, v162, v163
	v_add_f32_e32 v187, v164, v165
	ds_read_b128 v[158:161], v125 offset:39936
	s_waitcnt lgkmcnt(7)
	v_pk_fma_f32 v[162:163], v[104:105], v[130:131], 0 op_sel_hi:[1,1,0]
	v_pk_fma_f32 v[164:165], v[120:121], v[130:131], 0 op_sel_hi:[1,1,0]
	v_pk_fma_f32 v[162:163], v[102:103], v[132:133], v[162:163]
	v_pk_fma_f32 v[164:165], v[118:119], v[132:133], v[164:165]
	ds_read_b128 v[130:133], v125 offset:40960
	s_waitcnt lgkmcnt(7)
	v_pk_fma_f32 v[162:163], v[100:101], v[134:135], v[162:163]
	v_pk_fma_f32 v[164:165], v[116:117], v[134:135], v[164:165]
	v_pk_fma_f32 v[162:163], v[98:99], v[136:137], v[162:163]
	v_pk_fma_f32 v[164:165], v[114:115], v[136:137], v[164:165]
	ds_read_b128 v[134:137], v125 offset:41984
	s_waitcnt lgkmcnt(7)
	v_pk_fma_f32 v[162:163], v[96:97], v[138:139], v[162:163]
	v_pk_fma_f32 v[164:165], v[112:113], v[138:139], v[164:165]
	v_pk_fma_f32 v[162:163], v[94:95], v[140:141], v[162:163]
	v_pk_fma_f32 v[164:165], v[110:111], v[140:141], v[164:165]
	ds_read_b128 v[138:141], v125 offset:43008
	s_waitcnt lgkmcnt(7)
	v_pk_fma_f32 v[162:163], v[92:93], v[142:143], v[162:163]
	v_pk_fma_f32 v[164:165], v[108:109], v[142:143], v[164:165]
	v_pk_fma_f32 v[162:163], v[90:91], v[144:145], v[162:163]
	v_pk_fma_f32 v[164:165], v[106:107], v[144:145], v[164:165]
	v_add_f32_e32 v194, v162, v163
	v_add_f32_e32 v189, v164, v165
	ds_read_b128 v[142:145], v125 offset:44032
	s_waitcnt lgkmcnt(7)
	v_pk_fma_f32 v[162:163], v[104:105], v[146:147], 0 op_sel_hi:[1,1,0]
	v_pk_fma_f32 v[164:165], v[120:121], v[146:147], 0 op_sel_hi:[1,1,0]
	v_pk_fma_f32 v[162:163], v[102:103], v[148:149], v[162:163]
	v_pk_fma_f32 v[164:165], v[118:119], v[148:149], v[164:165]
	ds_read_b128 v[146:149], v125 offset:45056
	s_waitcnt lgkmcnt(7)
	v_pk_fma_f32 v[162:163], v[100:101], v[150:151], v[162:163]
	v_pk_fma_f32 v[164:165], v[116:117], v[150:151], v[164:165]
	v_pk_fma_f32 v[162:163], v[98:99], v[152:153], v[162:163]
	v_pk_fma_f32 v[164:165], v[114:115], v[152:153], v[164:165]
	ds_read_b128 v[150:153], v125 offset:46080
	s_waitcnt lgkmcnt(7)
	v_pk_fma_f32 v[162:163], v[96:97], v[154:155], v[162:163]
	v_pk_fma_f32 v[164:165], v[112:113], v[154:155], v[164:165]
	v_pk_fma_f32 v[162:163], v[94:95], v[156:157], v[162:163]
	v_pk_fma_f32 v[164:165], v[110:111], v[156:157], v[164:165]
	ds_read_b128 v[154:157], v125 offset:47104
	s_waitcnt lgkmcnt(7)
	v_pk_fma_f32 v[162:163], v[92:93], v[158:159], v[162:163]
	v_pk_fma_f32 v[164:165], v[108:109], v[158:159], v[164:165]
	v_pk_fma_f32 v[162:163], v[90:91], v[160:161], v[162:163]
	v_pk_fma_f32 v[164:165], v[106:107], v[160:161], v[164:165]
	v_add_f32_e32 v196, v162, v163
	v_add_f32_e32 v191, v164, v165
	ds_read_b128 v[158:161], v125 offset:48128
	s_waitcnt lgkmcnt(7)
	v_pk_fma_f32 v[162:163], v[104:105], v[130:131], 0 op_sel_hi:[1,1,0]
	v_pk_fma_f32 v[164:165], v[120:121], v[130:131], 0 op_sel_hi:[1,1,0]
	v_pk_fma_f32 v[162:163], v[102:103], v[132:133], v[162:163]
	v_pk_fma_f32 v[164:165], v[118:119], v[132:133], v[164:165]
	ds_read_b128 v[130:133], v125 offset:49152
	s_waitcnt lgkmcnt(7)
	v_pk_fma_f32 v[162:163], v[100:101], v[134:135], v[162:163]
	v_pk_fma_f32 v[164:165], v[116:117], v[134:135], v[164:165]
	v_pk_fma_f32 v[162:163], v[98:99], v[136:137], v[162:163]
	v_pk_fma_f32 v[164:165], v[114:115], v[136:137], v[164:165]
	ds_read_b128 v[134:137], v125 offset:50176
	s_waitcnt lgkmcnt(7)
	v_pk_fma_f32 v[162:163], v[96:97], v[138:139], v[162:163]
	v_pk_fma_f32 v[164:165], v[112:113], v[138:139], v[164:165]
	v_pk_fma_f32 v[162:163], v[94:95], v[140:141], v[162:163]
	v_pk_fma_f32 v[164:165], v[110:111], v[140:141], v[164:165]
	ds_read_b128 v[138:141], v125 offset:51200
	s_waitcnt lgkmcnt(7)
	v_pk_fma_f32 v[162:163], v[92:93], v[142:143], v[162:163]
	v_pk_fma_f32 v[164:165], v[108:109], v[142:143], v[164:165]
	v_pk_fma_f32 v[162:163], v[90:91], v[144:145], v[162:163]
	v_pk_fma_f32 v[164:165], v[106:107], v[144:145], v[164:165]
	v_add_f32_e32 v198, v162, v163
	v_add_f32_e32 v193, v164, v165
	ds_read_b128 v[142:145], v125 offset:52224
	s_waitcnt lgkmcnt(7)
	v_pk_fma_f32 v[162:163], v[104:105], v[146:147], 0 op_sel_hi:[1,1,0]
	v_pk_fma_f32 v[164:165], v[120:121], v[146:147], 0 op_sel_hi:[1,1,0]
	v_pk_fma_f32 v[162:163], v[102:103], v[148:149], v[162:163]
	v_pk_fma_f32 v[164:165], v[118:119], v[148:149], v[164:165]
	ds_read_b128 v[146:149], v125 offset:53248
	s_waitcnt lgkmcnt(7)
	v_pk_fma_f32 v[162:163], v[100:101], v[150:151], v[162:163]
	v_pk_fma_f32 v[164:165], v[116:117], v[150:151], v[164:165]
	v_pk_fma_f32 v[162:163], v[98:99], v[152:153], v[162:163]
	v_pk_fma_f32 v[164:165], v[114:115], v[152:153], v[164:165]
	ds_read_b128 v[150:153], v125 offset:54272
	s_waitcnt lgkmcnt(7)
	v_pk_fma_f32 v[162:163], v[96:97], v[154:155], v[162:163]
	v_pk_fma_f32 v[164:165], v[112:113], v[154:155], v[164:165]
	v_pk_fma_f32 v[162:163], v[94:95], v[156:157], v[162:163]
	v_pk_fma_f32 v[164:165], v[110:111], v[156:157], v[164:165]
	ds_read_b128 v[154:157], v125 offset:55296
	s_waitcnt lgkmcnt(7)
	v_pk_fma_f32 v[162:163], v[92:93], v[158:159], v[162:163]
	v_pk_fma_f32 v[164:165], v[108:109], v[158:159], v[164:165]
	v_pk_fma_f32 v[162:163], v[90:91], v[160:161], v[162:163]
	v_pk_fma_f32 v[164:165], v[106:107], v[160:161], v[164:165]
	v_add_f32_e32 v208, v162, v163
	v_add_f32_e32 v195, v164, v165
	ds_read_b128 v[158:161], v125 offset:56320
	s_waitcnt lgkmcnt(7)
	v_pk_fma_f32 v[162:163], v[104:105], v[130:131], 0 op_sel_hi:[1,1,0]
	v_pk_fma_f32 v[164:165], v[120:121], v[130:131], 0 op_sel_hi:[1,1,0]
	v_pk_fma_f32 v[162:163], v[102:103], v[132:133], v[162:163]
	v_pk_fma_f32 v[164:165], v[118:119], v[132:133], v[164:165]
	ds_read_b128 v[130:133], v125 offset:57344
	s_waitcnt lgkmcnt(7)
	v_pk_fma_f32 v[162:163], v[100:101], v[134:135], v[162:163]
	v_pk_fma_f32 v[164:165], v[116:117], v[134:135], v[164:165]
	v_pk_fma_f32 v[162:163], v[98:99], v[136:137], v[162:163]
	v_pk_fma_f32 v[164:165], v[114:115], v[136:137], v[164:165]
	ds_read_b128 v[134:137], v125 offset:58368
	s_waitcnt lgkmcnt(7)
	v_pk_fma_f32 v[162:163], v[96:97], v[138:139], v[162:163]
	v_pk_fma_f32 v[164:165], v[112:113], v[138:139], v[164:165]
	v_pk_fma_f32 v[162:163], v[94:95], v[140:141], v[162:163]
	v_pk_fma_f32 v[164:165], v[110:111], v[140:141], v[164:165]
	ds_read_b128 v[138:141], v125 offset:59392
	s_waitcnt lgkmcnt(7)
	v_pk_fma_f32 v[162:163], v[92:93], v[142:143], v[162:163]
	v_pk_fma_f32 v[164:165], v[108:109], v[142:143], v[164:165]
	v_pk_fma_f32 v[162:163], v[90:91], v[144:145], v[162:163]
	v_pk_fma_f32 v[164:165], v[106:107], v[144:145], v[164:165]
	v_add_f32_e32 v213, v162, v163
	v_add_f32_e32 v197, v164, v165
	ds_read_b128 v[142:145], v125 offset:60416
	s_waitcnt lgkmcnt(7)
	v_pk_fma_f32 v[162:163], v[104:105], v[146:147], 0 op_sel_hi:[1,1,0]
	v_pk_fma_f32 v[164:165], v[120:121], v[146:147], 0 op_sel_hi:[1,1,0]
	v_pk_fma_f32 v[162:163], v[102:103], v[148:149], v[162:163]
	v_pk_fma_f32 v[164:165], v[118:119], v[148:149], v[164:165]
	ds_read_b128 v[146:149], v125 offset:61440
	s_waitcnt lgkmcnt(7)
	v_pk_fma_f32 v[162:163], v[100:101], v[150:151], v[162:163]
	v_pk_fma_f32 v[164:165], v[116:117], v[150:151], v[164:165]
	v_pk_fma_f32 v[162:163], v[98:99], v[152:153], v[162:163]
	v_pk_fma_f32 v[164:165], v[114:115], v[152:153], v[164:165]
	ds_read_b128 v[150:153], v125 offset:62464
	s_waitcnt lgkmcnt(7)
	v_pk_fma_f32 v[162:163], v[96:97], v[154:155], v[162:163]
	v_pk_fma_f32 v[164:165], v[112:113], v[154:155], v[164:165]
	v_pk_fma_f32 v[162:163], v[94:95], v[156:157], v[162:163]
	v_pk_fma_f32 v[164:165], v[110:111], v[156:157], v[164:165]
	ds_read_b128 v[154:157], v125 offset:63488
	s_waitcnt lgkmcnt(7)
	v_pk_fma_f32 v[162:163], v[92:93], v[158:159], v[162:163]
	v_pk_fma_f32 v[164:165], v[108:109], v[158:159], v[164:165]
	v_pk_fma_f32 v[162:163], v[90:91], v[160:161], v[162:163]
	v_pk_fma_f32 v[164:165], v[106:107], v[160:161], v[164:165]
	v_add_f32_e32 v215, v162, v163
	v_add_f32_e32 v199, v164, v165
	ds_read_b128 v[158:161], v125 offset:64512
	s_waitcnt lgkmcnt(7)
	v_pk_fma_f32 v[162:163], v[104:105], v[130:131], 0 op_sel_hi:[1,1,0]
	v_pk_fma_f32 v[164:165], v[120:121], v[130:131], 0 op_sel_hi:[1,1,0]
	v_pk_fma_f32 v[162:163], v[102:103], v[132:133], v[162:163]
	v_pk_fma_f32 v[164:165], v[118:119], v[132:133], v[164:165]
	ds_read_b128 v[130:133], v129
	s_waitcnt lgkmcnt(7)
	v_pk_fma_f32 v[162:163], v[100:101], v[134:135], v[162:163]
	v_pk_fma_f32 v[164:165], v[116:117], v[134:135], v[164:165]
	v_pk_fma_f32 v[162:163], v[98:99], v[136:137], v[162:163]
	v_pk_fma_f32 v[164:165], v[114:115], v[136:137], v[164:165]
	ds_read_b128 v[134:137], v129 offset:1024
	s_waitcnt lgkmcnt(7)
	v_pk_fma_f32 v[162:163], v[96:97], v[138:139], v[162:163]
	v_pk_fma_f32 v[164:165], v[112:113], v[138:139], v[164:165]
	v_pk_fma_f32 v[162:163], v[94:95], v[140:141], v[162:163]
	v_pk_fma_f32 v[164:165], v[110:111], v[140:141], v[164:165]
	ds_read_b128 v[138:141], v129 offset:2048
	s_waitcnt lgkmcnt(7)
	v_pk_fma_f32 v[162:163], v[92:93], v[142:143], v[162:163]
	v_pk_fma_f32 v[164:165], v[108:109], v[142:143], v[164:165]
	v_pk_fma_f32 v[162:163], v[90:91], v[144:145], v[162:163]
	v_pk_fma_f32 v[164:165], v[106:107], v[144:145], v[164:165]
	v_add_f32_e32 v216, v162, v163
	v_add_f32_e32 v209, v164, v165
	ds_read_b128 v[142:145], v129 offset:3072
	s_waitcnt lgkmcnt(7)
	v_pk_fma_f32 v[162:163], v[104:105], v[146:147], 0 op_sel_hi:[1,1,0]
	v_pk_fma_f32 v[164:165], v[120:121], v[146:147], 0 op_sel_hi:[1,1,0]
	v_pk_fma_f32 v[162:163], v[102:103], v[148:149], v[162:163]
	v_pk_fma_f32 v[164:165], v[118:119], v[148:149], v[164:165]
	ds_read_b128 v[146:149], v129 offset:4096
	s_waitcnt lgkmcnt(7)
	v_pk_fma_f32 v[162:163], v[100:101], v[150:151], v[162:163]
	v_pk_fma_f32 v[164:165], v[116:117], v[150:151], v[164:165]
	v_pk_fma_f32 v[162:163], v[98:99], v[152:153], v[162:163]
	v_pk_fma_f32 v[164:165], v[114:115], v[152:153], v[164:165]
	ds_read_b128 v[150:153], v129 offset:5120
	s_waitcnt lgkmcnt(7)
	v_pk_fma_f32 v[162:163], v[96:97], v[154:155], v[162:163]
	v_pk_fma_f32 v[164:165], v[112:113], v[154:155], v[164:165]
	v_pk_fma_f32 v[162:163], v[94:95], v[156:157], v[162:163]
	v_pk_fma_f32 v[164:165], v[110:111], v[156:157], v[164:165]
	ds_read_b128 v[154:157], v129 offset:6144
	s_waitcnt lgkmcnt(7)
	v_pk_fma_f32 v[162:163], v[92:93], v[158:159], v[162:163]
	v_pk_fma_f32 v[164:165], v[108:109], v[158:159], v[164:165]
	v_pk_fma_f32 v[162:163], v[90:91], v[160:161], v[162:163]
	v_pk_fma_f32 v[164:165], v[106:107], v[160:161], v[164:165]
	v_add_f32_e32 v218, v162, v163
	v_add_f32_e32 v214, v164, v165
	ds_read_b128 v[158:161], v129 offset:7168
	s_waitcnt lgkmcnt(7)
	v_pk_fma_f32 v[162:163], v[104:105], v[130:131], 0 op_sel_hi:[1,1,0]
	v_pk_fma_f32 v[164:165], v[120:121], v[130:131], 0 op_sel_hi:[1,1,0]
	v_pk_fma_f32 v[162:163], v[102:103], v[132:133], v[162:163]
	v_pk_fma_f32 v[164:165], v[118:119], v[132:133], v[164:165]
	ds_read_b128 v[130:133], v129 offset:8192
	s_waitcnt lgkmcnt(7)
	v_pk_fma_f32 v[162:163], v[100:101], v[134:135], v[162:163]
	v_pk_fma_f32 v[164:165], v[116:117], v[134:135], v[164:165]
	v_pk_fma_f32 v[162:163], v[98:99], v[136:137], v[162:163]
	v_pk_fma_f32 v[164:165], v[114:115], v[136:137], v[164:165]
	ds_read_b128 v[134:137], v129 offset:9216
	s_waitcnt lgkmcnt(7)
	v_pk_fma_f32 v[162:163], v[96:97], v[138:139], v[162:163]
	v_pk_fma_f32 v[164:165], v[112:113], v[138:139], v[164:165]
	v_pk_fma_f32 v[162:163], v[94:95], v[140:141], v[162:163]
	v_pk_fma_f32 v[164:165], v[110:111], v[140:141], v[164:165]
	ds_read_b128 v[138:141], v129 offset:10240
	s_waitcnt lgkmcnt(7)
	v_pk_fma_f32 v[162:163], v[92:93], v[142:143], v[162:163]
	v_pk_fma_f32 v[164:165], v[108:109], v[142:143], v[164:165]
	v_pk_fma_f32 v[162:163], v[90:91], v[144:145], v[162:163]
	v_pk_fma_f32 v[164:165], v[106:107], v[144:145], v[164:165]
	v_add_f32_e32 v221, v162, v163
	v_add_f32_e32 v217, v164, v165
	ds_read_b128 v[142:145], v129 offset:11264
	s_waitcnt lgkmcnt(7)
	v_pk_fma_f32 v[162:163], v[104:105], v[146:147], 0 op_sel_hi:[1,1,0]
	v_pk_fma_f32 v[164:165], v[120:121], v[146:147], 0 op_sel_hi:[1,1,0]
	v_pk_fma_f32 v[162:163], v[102:103], v[148:149], v[162:163]
	v_pk_fma_f32 v[164:165], v[118:119], v[148:149], v[164:165]
	ds_read_b128 v[146:149], v129 offset:12288
	s_waitcnt lgkmcnt(7)
	v_pk_fma_f32 v[162:163], v[100:101], v[150:151], v[162:163]
	v_pk_fma_f32 v[164:165], v[116:117], v[150:151], v[164:165]
	v_pk_fma_f32 v[162:163], v[98:99], v[152:153], v[162:163]
	v_pk_fma_f32 v[164:165], v[114:115], v[152:153], v[164:165]
	ds_read_b128 v[150:153], v129 offset:13312
	s_waitcnt lgkmcnt(7)
	v_pk_fma_f32 v[162:163], v[96:97], v[154:155], v[162:163]
	v_pk_fma_f32 v[164:165], v[112:113], v[154:155], v[164:165]
	v_pk_fma_f32 v[162:163], v[94:95], v[156:157], v[162:163]
	v_pk_fma_f32 v[164:165], v[110:111], v[156:157], v[164:165]
	ds_read_b128 v[154:157], v129 offset:14336
	s_waitcnt lgkmcnt(7)
	v_pk_fma_f32 v[162:163], v[92:93], v[158:159], v[162:163]
	v_pk_fma_f32 v[164:165], v[108:109], v[158:159], v[164:165]
	v_pk_fma_f32 v[162:163], v[90:91], v[160:161], v[162:163]
	v_pk_fma_f32 v[164:165], v[106:107], v[160:161], v[164:165]
	v_add_f32_e32 v223, v162, v163
	v_add_f32_e32 v219, v164, v165
	ds_read_b128 v[158:161], v129 offset:15360
	s_waitcnt lgkmcnt(7)
	v_pk_fma_f32 v[162:163], v[104:105], v[130:131], 0 op_sel_hi:[1,1,0]
	v_pk_fma_f32 v[164:165], v[120:121], v[130:131], 0 op_sel_hi:[1,1,0]
	v_pk_fma_f32 v[162:163], v[102:103], v[132:133], v[162:163]
	v_pk_fma_f32 v[164:165], v[118:119], v[132:133], v[164:165]
	ds_read_b128 v[130:133], v129 offset:16384
	s_waitcnt lgkmcnt(7)
	v_pk_fma_f32 v[162:163], v[100:101], v[134:135], v[162:163]
	v_pk_fma_f32 v[164:165], v[116:117], v[134:135], v[164:165]
	v_pk_fma_f32 v[162:163], v[98:99], v[136:137], v[162:163]
	v_pk_fma_f32 v[164:165], v[114:115], v[136:137], v[164:165]
	ds_read_b128 v[134:137], v129 offset:17408
	s_waitcnt lgkmcnt(7)
	v_pk_fma_f32 v[162:163], v[96:97], v[138:139], v[162:163]
	v_pk_fma_f32 v[164:165], v[112:113], v[138:139], v[164:165]
	v_pk_fma_f32 v[162:163], v[94:95], v[140:141], v[162:163]
	v_pk_fma_f32 v[164:165], v[110:111], v[140:141], v[164:165]
	ds_read_b128 v[138:141], v129 offset:18432
	s_waitcnt lgkmcnt(7)
	v_pk_fma_f32 v[162:163], v[92:93], v[142:143], v[162:163]
	v_pk_fma_f32 v[164:165], v[108:109], v[142:143], v[164:165]
	v_pk_fma_f32 v[162:163], v[90:91], v[144:145], v[162:163]
	v_pk_fma_f32 v[164:165], v[106:107], v[144:145], v[164:165]
	v_add_f32_e32 v225, v162, v163
	v_add_f32_e32 v220, v164, v165
	ds_read_b128 v[142:145], v129 offset:19456
	s_waitcnt lgkmcnt(7)
	v_pk_fma_f32 v[162:163], v[104:105], v[146:147], 0 op_sel_hi:[1,1,0]
	v_pk_fma_f32 v[164:165], v[120:121], v[146:147], 0 op_sel_hi:[1,1,0]
	v_pk_fma_f32 v[162:163], v[102:103], v[148:149], v[162:163]
	v_pk_fma_f32 v[164:165], v[118:119], v[148:149], v[164:165]
	ds_read_b128 v[146:149], v129 offset:20480
	s_waitcnt lgkmcnt(7)
	v_pk_fma_f32 v[162:163], v[100:101], v[150:151], v[162:163]
	v_pk_fma_f32 v[164:165], v[116:117], v[150:151], v[164:165]
	v_pk_fma_f32 v[162:163], v[98:99], v[152:153], v[162:163]
	v_pk_fma_f32 v[164:165], v[114:115], v[152:153], v[164:165]
	ds_read_b128 v[150:153], v129 offset:21504
	s_waitcnt lgkmcnt(7)
	v_pk_fma_f32 v[162:163], v[96:97], v[154:155], v[162:163]
	v_pk_fma_f32 v[164:165], v[112:113], v[154:155], v[164:165]
	v_pk_fma_f32 v[162:163], v[94:95], v[156:157], v[162:163]
	v_pk_fma_f32 v[164:165], v[110:111], v[156:157], v[164:165]
	ds_read_b128 v[154:157], v129 offset:22528
	s_waitcnt lgkmcnt(7)
	v_pk_fma_f32 v[162:163], v[92:93], v[158:159], v[162:163]
	v_pk_fma_f32 v[164:165], v[108:109], v[158:159], v[164:165]
	v_pk_fma_f32 v[162:163], v[90:91], v[160:161], v[162:163]
	v_pk_fma_f32 v[164:165], v[106:107], v[160:161], v[164:165]
	v_add_f32_e32 v227, v162, v163
	v_add_f32_e32 v222, v164, v165
	ds_read_b128 v[158:161], v129 offset:23552
	s_waitcnt lgkmcnt(7)
	v_pk_fma_f32 v[162:163], v[104:105], v[130:131], 0 op_sel_hi:[1,1,0]
	v_pk_fma_f32 v[164:165], v[120:121], v[130:131], 0 op_sel_hi:[1,1,0]
	v_pk_fma_f32 v[162:163], v[102:103], v[132:133], v[162:163]
	v_pk_fma_f32 v[164:165], v[118:119], v[132:133], v[164:165]
	ds_read_b128 v[130:133], v129 offset:24576
	s_waitcnt lgkmcnt(7)
	v_pk_fma_f32 v[162:163], v[100:101], v[134:135], v[162:163]
	v_pk_fma_f32 v[164:165], v[116:117], v[134:135], v[164:165]
	v_pk_fma_f32 v[162:163], v[98:99], v[136:137], v[162:163]
	v_pk_fma_f32 v[164:165], v[114:115], v[136:137], v[164:165]
	ds_read_b128 v[134:137], v129 offset:25600
	s_waitcnt lgkmcnt(7)
	v_pk_fma_f32 v[162:163], v[96:97], v[138:139], v[162:163]
	v_pk_fma_f32 v[164:165], v[112:113], v[138:139], v[164:165]
	v_pk_fma_f32 v[162:163], v[94:95], v[140:141], v[162:163]
	v_pk_fma_f32 v[164:165], v[110:111], v[140:141], v[164:165]
	ds_read_b128 v[138:141], v129 offset:26624
	s_waitcnt lgkmcnt(7)
	v_pk_fma_f32 v[162:163], v[92:93], v[142:143], v[162:163]
	v_pk_fma_f32 v[164:165], v[108:109], v[142:143], v[164:165]
	v_pk_fma_f32 v[162:163], v[90:91], v[144:145], v[162:163]
	v_pk_fma_f32 v[164:165], v[106:107], v[144:145], v[164:165]
	v_add_f32_e32 v229, v162, v163
	v_add_f32_e32 v224, v164, v165
	ds_read_b128 v[142:145], v129 offset:27648
	s_waitcnt lgkmcnt(7)
	v_pk_fma_f32 v[162:163], v[104:105], v[146:147], 0 op_sel_hi:[1,1,0]
	v_pk_fma_f32 v[164:165], v[120:121], v[146:147], 0 op_sel_hi:[1,1,0]
	v_pk_fma_f32 v[162:163], v[102:103], v[148:149], v[162:163]
	v_pk_fma_f32 v[164:165], v[118:119], v[148:149], v[164:165]
	ds_read_b128 v[146:149], v129 offset:28672
	s_waitcnt lgkmcnt(7)
	v_pk_fma_f32 v[162:163], v[100:101], v[150:151], v[162:163]
	v_pk_fma_f32 v[164:165], v[116:117], v[150:151], v[164:165]
	v_pk_fma_f32 v[162:163], v[98:99], v[152:153], v[162:163]
	v_pk_fma_f32 v[164:165], v[114:115], v[152:153], v[164:165]
	ds_read_b128 v[150:153], v129 offset:29696
	s_waitcnt lgkmcnt(7)
	v_pk_fma_f32 v[162:163], v[96:97], v[154:155], v[162:163]
	v_pk_fma_f32 v[164:165], v[112:113], v[154:155], v[164:165]
	v_pk_fma_f32 v[162:163], v[94:95], v[156:157], v[162:163]
	v_pk_fma_f32 v[164:165], v[110:111], v[156:157], v[164:165]
	ds_read_b128 v[154:157], v129 offset:30720
	s_waitcnt lgkmcnt(7)
	v_pk_fma_f32 v[162:163], v[92:93], v[158:159], v[162:163]
	v_pk_fma_f32 v[164:165], v[108:109], v[158:159], v[164:165]
	v_pk_fma_f32 v[162:163], v[90:91], v[160:161], v[162:163]
	v_pk_fma_f32 v[164:165], v[106:107], v[160:161], v[164:165]
	v_add_f32_e32 v231, v162, v163
	v_add_f32_e32 v226, v164, v165
	ds_read_b128 v[158:161], v129 offset:31744
	s_waitcnt lgkmcnt(7)
	v_pk_fma_f32 v[162:163], v[104:105], v[130:131], 0 op_sel_hi:[1,1,0]
	v_pk_fma_f32 v[164:165], v[120:121], v[130:131], 0 op_sel_hi:[1,1,0]
	v_pk_fma_f32 v[162:163], v[102:103], v[132:133], v[162:163]
	v_pk_fma_f32 v[164:165], v[118:119], v[132:133], v[164:165]
	ds_read_b128 v[130:133], v129 offset:32768
	s_waitcnt lgkmcnt(7)
	v_pk_fma_f32 v[162:163], v[100:101], v[134:135], v[162:163]
	v_pk_fma_f32 v[164:165], v[116:117], v[134:135], v[164:165]
	v_pk_fma_f32 v[162:163], v[98:99], v[136:137], v[162:163]
	v_pk_fma_f32 v[164:165], v[114:115], v[136:137], v[164:165]
	ds_read_b128 v[134:137], v129 offset:33792
	s_waitcnt lgkmcnt(7)
	v_pk_fma_f32 v[162:163], v[96:97], v[138:139], v[162:163]
	v_pk_fma_f32 v[164:165], v[112:113], v[138:139], v[164:165]
	v_pk_fma_f32 v[162:163], v[94:95], v[140:141], v[162:163]
	v_pk_fma_f32 v[164:165], v[110:111], v[140:141], v[164:165]
	ds_read_b128 v[138:141], v129 offset:34816
	s_waitcnt lgkmcnt(7)
	v_pk_fma_f32 v[162:163], v[92:93], v[142:143], v[162:163]
	v_pk_fma_f32 v[164:165], v[108:109], v[142:143], v[164:165]
	v_pk_fma_f32 v[162:163], v[90:91], v[144:145], v[162:163]
	v_pk_fma_f32 v[164:165], v[106:107], v[144:145], v[164:165]
	v_add_f32_e32 v233, v162, v163
	v_add_f32_e32 v228, v164, v165
	ds_read_b128 v[142:145], v129 offset:35840
	s_waitcnt lgkmcnt(7)
	v_pk_fma_f32 v[162:163], v[104:105], v[146:147], 0 op_sel_hi:[1,1,0]
	v_pk_fma_f32 v[164:165], v[120:121], v[146:147], 0 op_sel_hi:[1,1,0]
	v_pk_fma_f32 v[162:163], v[102:103], v[148:149], v[162:163]
	v_pk_fma_f32 v[164:165], v[118:119], v[148:149], v[164:165]
	ds_read_b128 v[146:149], v129 offset:36864
	s_waitcnt lgkmcnt(7)
	v_pk_fma_f32 v[162:163], v[100:101], v[150:151], v[162:163]
	v_pk_fma_f32 v[164:165], v[116:117], v[150:151], v[164:165]
	v_pk_fma_f32 v[162:163], v[98:99], v[152:153], v[162:163]
	v_pk_fma_f32 v[164:165], v[114:115], v[152:153], v[164:165]
	ds_read_b128 v[150:153], v129 offset:37888
	s_waitcnt lgkmcnt(7)
	v_pk_fma_f32 v[162:163], v[96:97], v[154:155], v[162:163]
	v_pk_fma_f32 v[164:165], v[112:113], v[154:155], v[164:165]
	v_pk_fma_f32 v[162:163], v[94:95], v[156:157], v[162:163]
	v_pk_fma_f32 v[164:165], v[110:111], v[156:157], v[164:165]
	ds_read_b128 v[154:157], v129 offset:38912
	s_waitcnt lgkmcnt(7)
	v_pk_fma_f32 v[162:163], v[92:93], v[158:159], v[162:163]
	v_pk_fma_f32 v[164:165], v[108:109], v[158:159], v[164:165]
	v_pk_fma_f32 v[162:163], v[90:91], v[160:161], v[162:163]
	v_pk_fma_f32 v[164:165], v[106:107], v[160:161], v[164:165]
	v_add_f32_e32 v235, v162, v163
	v_add_f32_e32 v230, v164, v165
	ds_read_b128 v[158:161], v129 offset:39936
	s_waitcnt lgkmcnt(7)
	v_pk_fma_f32 v[162:163], v[104:105], v[130:131], 0 op_sel_hi:[1,1,0]
	v_pk_fma_f32 v[164:165], v[120:121], v[130:131], 0 op_sel_hi:[1,1,0]
	v_pk_fma_f32 v[162:163], v[102:103], v[132:133], v[162:163]
	v_pk_fma_f32 v[164:165], v[118:119], v[132:133], v[164:165]
	ds_read_b128 v[130:133], v129 offset:40960
	s_waitcnt lgkmcnt(7)
	v_pk_fma_f32 v[162:163], v[100:101], v[134:135], v[162:163]
	v_pk_fma_f32 v[164:165], v[116:117], v[134:135], v[164:165]
	v_pk_fma_f32 v[162:163], v[98:99], v[136:137], v[162:163]
	v_pk_fma_f32 v[164:165], v[114:115], v[136:137], v[164:165]
	ds_read_b128 v[134:137], v129 offset:41984
	s_waitcnt lgkmcnt(7)
	v_pk_fma_f32 v[162:163], v[96:97], v[138:139], v[162:163]
	v_pk_fma_f32 v[164:165], v[112:113], v[138:139], v[164:165]
	v_pk_fma_f32 v[162:163], v[94:95], v[140:141], v[162:163]
	v_pk_fma_f32 v[164:165], v[110:111], v[140:141], v[164:165]
	ds_read_b128 v[138:141], v129 offset:43008
	s_waitcnt lgkmcnt(7)
	v_pk_fma_f32 v[162:163], v[92:93], v[142:143], v[162:163]
	v_pk_fma_f32 v[164:165], v[108:109], v[142:143], v[164:165]
	v_pk_fma_f32 v[162:163], v[90:91], v[144:145], v[162:163]
	v_pk_fma_f32 v[164:165], v[106:107], v[144:145], v[164:165]
	v_add_f32_e32 v237, v162, v163
	v_add_f32_e32 v232, v164, v165
	ds_read_b128 v[142:145], v129 offset:44032
	s_waitcnt lgkmcnt(7)
	v_pk_fma_f32 v[162:163], v[104:105], v[146:147], 0 op_sel_hi:[1,1,0]
	v_pk_fma_f32 v[164:165], v[120:121], v[146:147], 0 op_sel_hi:[1,1,0]
	v_pk_fma_f32 v[162:163], v[102:103], v[148:149], v[162:163]
	v_pk_fma_f32 v[164:165], v[118:119], v[148:149], v[164:165]
	ds_read_b128 v[146:149], v129 offset:45056
	s_waitcnt lgkmcnt(7)
	v_pk_fma_f32 v[162:163], v[100:101], v[150:151], v[162:163]
	v_pk_fma_f32 v[164:165], v[116:117], v[150:151], v[164:165]
	v_pk_fma_f32 v[162:163], v[98:99], v[152:153], v[162:163]
	v_pk_fma_f32 v[164:165], v[114:115], v[152:153], v[164:165]
	ds_read_b128 v[150:153], v129 offset:46080
	s_waitcnt lgkmcnt(7)
	v_pk_fma_f32 v[162:163], v[96:97], v[154:155], v[162:163]
	v_pk_fma_f32 v[164:165], v[112:113], v[154:155], v[164:165]
	v_pk_fma_f32 v[162:163], v[94:95], v[156:157], v[162:163]
	v_pk_fma_f32 v[164:165], v[110:111], v[156:157], v[164:165]
	ds_read_b128 v[154:157], v129 offset:47104
	s_waitcnt lgkmcnt(7)
	v_pk_fma_f32 v[162:163], v[92:93], v[158:159], v[162:163]
	v_pk_fma_f32 v[164:165], v[108:109], v[158:159], v[164:165]
	v_pk_fma_f32 v[162:163], v[90:91], v[160:161], v[162:163]
	v_pk_fma_f32 v[164:165], v[106:107], v[160:161], v[164:165]
	v_add_f32_e32 v239, v162, v163
	v_add_f32_e32 v234, v164, v165
	ds_read_b128 v[158:161], v129 offset:48128
	s_waitcnt lgkmcnt(7)
	v_pk_fma_f32 v[162:163], v[104:105], v[130:131], 0 op_sel_hi:[1,1,0]
	v_pk_fma_f32 v[164:165], v[120:121], v[130:131], 0 op_sel_hi:[1,1,0]
	v_pk_fma_f32 v[162:163], v[102:103], v[132:133], v[162:163]
	v_pk_fma_f32 v[164:165], v[118:119], v[132:133], v[164:165]
	ds_read_b128 v[130:133], v129 offset:49152
	s_waitcnt lgkmcnt(7)
	v_pk_fma_f32 v[162:163], v[100:101], v[134:135], v[162:163]
	v_pk_fma_f32 v[164:165], v[116:117], v[134:135], v[164:165]
	v_pk_fma_f32 v[162:163], v[98:99], v[136:137], v[162:163]
	v_pk_fma_f32 v[164:165], v[114:115], v[136:137], v[164:165]
	ds_read_b128 v[134:137], v129 offset:50176
	s_waitcnt lgkmcnt(7)
	v_pk_fma_f32 v[162:163], v[96:97], v[138:139], v[162:163]
	v_pk_fma_f32 v[164:165], v[112:113], v[138:139], v[164:165]
	v_pk_fma_f32 v[162:163], v[94:95], v[140:141], v[162:163]
	v_pk_fma_f32 v[164:165], v[110:111], v[140:141], v[164:165]
	ds_read_b128 v[138:141], v129 offset:51200
	s_waitcnt lgkmcnt(7)
	v_pk_fma_f32 v[162:163], v[92:93], v[142:143], v[162:163]
	v_pk_fma_f32 v[164:165], v[108:109], v[142:143], v[164:165]
	v_pk_fma_f32 v[162:163], v[90:91], v[144:145], v[162:163]
	v_pk_fma_f32 v[164:165], v[106:107], v[144:145], v[164:165]
	v_add_f32_e32 v241, v162, v163
	v_add_f32_e32 v236, v164, v165
	ds_read_b128 v[142:145], v129 offset:52224
	s_waitcnt lgkmcnt(7)
	v_pk_fma_f32 v[162:163], v[104:105], v[146:147], 0 op_sel_hi:[1,1,0]
	v_pk_fma_f32 v[164:165], v[120:121], v[146:147], 0 op_sel_hi:[1,1,0]
	v_pk_fma_f32 v[162:163], v[102:103], v[148:149], v[162:163]
	v_pk_fma_f32 v[164:165], v[118:119], v[148:149], v[164:165]
	ds_read_b128 v[146:149], v129 offset:53248
	s_waitcnt lgkmcnt(7)
	v_pk_fma_f32 v[162:163], v[100:101], v[150:151], v[162:163]
	v_pk_fma_f32 v[164:165], v[116:117], v[150:151], v[164:165]
	v_pk_fma_f32 v[162:163], v[98:99], v[152:153], v[162:163]
	v_pk_fma_f32 v[164:165], v[114:115], v[152:153], v[164:165]
	ds_read_b128 v[150:153], v129 offset:54272
	s_waitcnt lgkmcnt(7)
	v_pk_fma_f32 v[162:163], v[96:97], v[154:155], v[162:163]
	v_pk_fma_f32 v[164:165], v[112:113], v[154:155], v[164:165]
	v_pk_fma_f32 v[162:163], v[94:95], v[156:157], v[162:163]
	v_pk_fma_f32 v[164:165], v[110:111], v[156:157], v[164:165]
	ds_read_b128 v[154:157], v129 offset:55296
	s_waitcnt lgkmcnt(7)
	v_pk_fma_f32 v[162:163], v[92:93], v[158:159], v[162:163]
	v_pk_fma_f32 v[164:165], v[108:109], v[158:159], v[164:165]
	v_pk_fma_f32 v[162:163], v[90:91], v[160:161], v[162:163]
	v_pk_fma_f32 v[164:165], v[106:107], v[160:161], v[164:165]
	v_add_f32_e32 v243, v162, v163
	v_add_f32_e32 v238, v164, v165
	ds_read_b128 v[158:161], v129 offset:56320
	s_waitcnt lgkmcnt(7)
	v_pk_fma_f32 v[162:163], v[104:105], v[130:131], 0 op_sel_hi:[1,1,0]
	v_pk_fma_f32 v[164:165], v[120:121], v[130:131], 0 op_sel_hi:[1,1,0]
	v_pk_fma_f32 v[162:163], v[102:103], v[132:133], v[162:163]
	v_pk_fma_f32 v[164:165], v[118:119], v[132:133], v[164:165]
	ds_read_b128 v[130:133], v129 offset:57344
	s_waitcnt lgkmcnt(7)
	v_pk_fma_f32 v[162:163], v[100:101], v[134:135], v[162:163]
	v_pk_fma_f32 v[164:165], v[116:117], v[134:135], v[164:165]
	v_pk_fma_f32 v[162:163], v[98:99], v[136:137], v[162:163]
	v_pk_fma_f32 v[164:165], v[114:115], v[136:137], v[164:165]
	ds_read_b128 v[134:137], v129 offset:58368
	s_waitcnt lgkmcnt(7)
	v_pk_fma_f32 v[162:163], v[96:97], v[138:139], v[162:163]
	v_pk_fma_f32 v[164:165], v[112:113], v[138:139], v[164:165]
	v_pk_fma_f32 v[162:163], v[94:95], v[140:141], v[162:163]
	v_pk_fma_f32 v[164:165], v[110:111], v[140:141], v[164:165]
	ds_read_b128 v[138:141], v129 offset:59392
	s_waitcnt lgkmcnt(7)
	v_pk_fma_f32 v[162:163], v[92:93], v[142:143], v[162:163]
	v_pk_fma_f32 v[164:165], v[108:109], v[142:143], v[164:165]
	v_pk_fma_f32 v[162:163], v[90:91], v[144:145], v[162:163]
	v_pk_fma_f32 v[164:165], v[106:107], v[144:145], v[164:165]
	v_add_f32_e32 v245, v162, v163
	v_add_f32_e32 v240, v164, v165
	ds_read_b128 v[142:145], v129 offset:60416
	s_waitcnt lgkmcnt(7)
	v_pk_fma_f32 v[162:163], v[104:105], v[146:147], 0 op_sel_hi:[1,1,0]
	v_pk_fma_f32 v[164:165], v[120:121], v[146:147], 0 op_sel_hi:[1,1,0]
	v_pk_fma_f32 v[162:163], v[102:103], v[148:149], v[162:163]
	v_pk_fma_f32 v[164:165], v[118:119], v[148:149], v[164:165]
	ds_read_b128 v[146:149], v129 offset:61440
	s_waitcnt lgkmcnt(7)
	v_pk_fma_f32 v[162:163], v[100:101], v[150:151], v[162:163]
	v_pk_fma_f32 v[164:165], v[116:117], v[150:151], v[164:165]
	v_pk_fma_f32 v[162:163], v[98:99], v[152:153], v[162:163]
	v_pk_fma_f32 v[164:165], v[114:115], v[152:153], v[164:165]
	ds_read_b128 v[150:153], v129 offset:62464
	s_waitcnt lgkmcnt(7)
	v_pk_fma_f32 v[162:163], v[96:97], v[154:155], v[162:163]
	v_pk_fma_f32 v[164:165], v[112:113], v[154:155], v[164:165]
	v_pk_fma_f32 v[162:163], v[94:95], v[156:157], v[162:163]
	v_pk_fma_f32 v[164:165], v[110:111], v[156:157], v[164:165]
	ds_read_b128 v[154:157], v129 offset:63488
	s_waitcnt lgkmcnt(7)
	v_pk_fma_f32 v[162:163], v[92:93], v[158:159], v[162:163]
	v_pk_fma_f32 v[164:165], v[108:109], v[158:159], v[164:165]
	v_pk_fma_f32 v[162:163], v[90:91], v[160:161], v[162:163]
	v_pk_fma_f32 v[164:165], v[106:107], v[160:161], v[164:165]
	v_add_f32_e32 v212, v162, v163
	v_add_f32_e32 v242, v164, v165
	ds_read_b128 v[158:161], v129 offset:64512
	s_waitcnt lgkmcnt(7)
	v_pk_fma_f32 v[162:163], v[104:105], v[130:131], 0 op_sel_hi:[1,1,0]
	v_pk_fma_f32 v[164:165], v[120:121], v[130:131], 0 op_sel_hi:[1,1,0]
	v_pk_fma_f32 v[162:163], v[102:103], v[132:133], v[162:163]
	v_pk_fma_f32 v[164:165], v[118:119], v[132:133], v[164:165]
	s_waitcnt lgkmcnt(6)
	v_pk_fma_f32 v[162:163], v[100:101], v[134:135], v[162:163]
	v_pk_fma_f32 v[164:165], v[116:117], v[134:135], v[164:165]
	v_pk_fma_f32 v[162:163], v[98:99], v[136:137], v[162:163]
	v_pk_fma_f32 v[164:165], v[114:115], v[136:137], v[164:165]
	s_waitcnt lgkmcnt(5)
	v_pk_fma_f32 v[162:163], v[96:97], v[138:139], v[162:163]
	v_pk_fma_f32 v[164:165], v[112:113], v[138:139], v[164:165]
	v_pk_fma_f32 v[162:163], v[94:95], v[140:141], v[162:163]
	v_pk_fma_f32 v[164:165], v[110:111], v[140:141], v[164:165]
	s_waitcnt lgkmcnt(4)
	v_pk_fma_f32 v[162:163], v[92:93], v[142:143], v[162:163]
	v_pk_fma_f32 v[164:165], v[108:109], v[142:143], v[164:165]
	v_pk_fma_f32 v[162:163], v[90:91], v[144:145], v[162:163]
	v_pk_fma_f32 v[164:165], v[106:107], v[144:145], v[164:165]
	v_add_f32_e32 v210, v162, v163
	v_add_f32_e32 v244, v164, v165
	s_waitcnt lgkmcnt(3)
	v_pk_fma_f32 v[162:163], v[104:105], v[146:147], 0 op_sel_hi:[1,1,0]
	v_pk_fma_f32 v[164:165], v[120:121], v[146:147], 0 op_sel_hi:[1,1,0]
	v_pk_fma_f32 v[162:163], v[102:103], v[148:149], v[162:163]
	v_pk_fma_f32 v[164:165], v[118:119], v[148:149], v[164:165]
	s_waitcnt lgkmcnt(2)
	v_pk_fma_f32 v[162:163], v[100:101], v[150:151], v[162:163]
	v_pk_fma_f32 v[164:165], v[116:117], v[150:151], v[164:165]
	v_pk_fma_f32 v[162:163], v[98:99], v[152:153], v[162:163]
	v_pk_fma_f32 v[164:165], v[114:115], v[152:153], v[164:165]
	s_waitcnt lgkmcnt(1)
	v_pk_fma_f32 v[162:163], v[96:97], v[154:155], v[162:163]
	v_pk_fma_f32 v[164:165], v[112:113], v[154:155], v[164:165]
	v_pk_fma_f32 v[162:163], v[94:95], v[156:157], v[162:163]
	v_pk_fma_f32 v[164:165], v[110:111], v[156:157], v[164:165]
	s_waitcnt lgkmcnt(0)
	v_pk_fma_f32 v[162:163], v[92:93], v[158:159], v[162:163]
	v_pk_fma_f32 v[164:165], v[108:109], v[158:159], v[164:165]
	v_pk_fma_f32 v[162:163], v[90:91], v[160:161], v[162:163]
	v_pk_fma_f32 v[164:165], v[106:107], v[160:161], v[164:165]
	v_add_f32_e32 v90, v162, v163
	v_add_f32_e32 v91, v164, v165
	s_nop 1
	v_permlane32_swap_b32_e32 v178, v221
	s_nop 1
	v_permlane32_swap_b32_e32 v180, v223
	s_nop 1
	v_permlane32_swap_b32_e32 v182, v225
	s_nop 1
	v_permlane32_swap_b32_e32 v184, v227
	s_nop 1
	v_permlane32_swap_b32_e32 v186, v229
	s_nop 1
	v_permlane32_swap_b32_e32 v188, v231
	s_nop 1
	v_permlane32_swap_b32_e32 v190, v233
	s_nop 1
	v_permlane32_swap_b32_e32 v192, v235
	s_nop 1
	v_permlane32_swap_b32_e32 v194, v237
	s_nop 1
	v_permlane32_swap_b32_e32 v196, v239
	v_add_f32_e32 v92, v178, v221
	v_permlane32_swap_b32_e32 v198, v241
	v_add_f32_e32 v93, v180, v223
	v_add_f32_e32 v94, v182, v225
	v_add_f32_e32 v95, v184, v227
	v_permlane32_swap_b32_e32 v208, v243
	v_add_f32_e32 v96, v186, v229
	v_add_f32_e32 v97, v188, v231
	v_add_f32_e32 v98, v190, v233
	v_permlane32_swap_b32_e32 v213, v245
	v_add_f32_e32 v99, v192, v235
	v_add_f32_e32 v100, v194, v237
	v_add_f32_e32 v101, v196, v239
	v_permlane32_swap_b32_e32 v215, v212
	v_add_f32_e32 v102, v198, v241
	v_add_f32_e32 v103, v208, v243
	v_add_f32_e32 v104, v213, v245
	v_permlane32_swap_b32_e32 v216, v210
	v_add_f32_e32 v105, v215, v212
	v_add_f32_e32 v106, v216, v210
	v_cndmask_b32_e64 v107, v90, v218, s[8:9]
	v_cndmask_b32_e64 v90, v218, v90, s[8:9]
	v_mov_b32_e32 v108, v90
	s_nop 1
	v_permlane32_swap_b32_e32 v90, v108
	v_cndmask_b32_e64 v90, v90, v108, s[8:9]
	v_add_f32_e32 v90, v107, v90
	v_cndmask_b32_e64 v107, v100, v92, s[10:11]
	v_cndmask_b32_e64 v92, v92, v100, s[10:11]
	v_permlane16_swap_b32_e32 v93, v101
	ds_swizzle_b32 v92, v92 offset:swizzle(SWAP,16)
	s_waitcnt lgkmcnt(1)
	v_add_f32_e32 v93, v93, v101
	v_permlane16_swap_b32_e32 v94, v102
	s_waitcnt lgkmcnt(0)
	v_add_f32_e32 v92, v107, v92
	s_waitcnt lgkmcnt(0)
	v_add_f32_e32 v94, v94, v102
	v_permlane16_swap_b32_e32 v95, v103
	s_waitcnt lgkmcnt(0)
	v_add_f32_e32 v95, v95, v103
	v_permlane16_swap_b32_e32 v96, v104
	s_waitcnt lgkmcnt(0)
	v_add_f32_e32 v96, v96, v104
	v_permlane16_swap_b32_e32 v97, v105
	s_waitcnt lgkmcnt(0)
	v_add_f32_e32 v97, v97, v105
	v_permlane16_swap_b32_e32 v98, v106
	s_waitcnt lgkmcnt(0)
	v_add_f32_e32 v98, v98, v106
	v_cndmask_b32_e64 v100, v90, v99, s[10:11]
	v_cndmask_b32_e64 v90, v99, v90, s[10:11]
	v_cndmask_b32_e64 v99, v96, v92, s[12:13]
	v_cndmask_b32_e64 v92, v92, v96, s[12:13]
	v_cndmask_b32_e64 v96, v97, v93, s[12:13]
	v_cndmask_b32_e64 v93, v93, v97, s[12:13]
	s_nop 1
	v_mov_b32_dpp v93, v93 row_ror:8 row_mask:0xf bank_mask:0xf
	ds_swizzle_b32 v90, v90 offset:swizzle(SWAP,16)
	s_nop 1
	v_mov_b32_dpp v92, v92 row_ror:8 row_mask:0xf bank_mask:0xf
	s_waitcnt lgkmcnt(1)
	v_add_f32_e32 v93, v96, v93
	v_cndmask_b32_e64 v96, v98, v94, s[12:13]
	v_cndmask_b32_e64 v94, v94, v98, s[12:13]
	s_nop 1
	v_mov_b32_dpp v94, v94 row_ror:8 row_mask:0xf bank_mask:0xf
	s_waitcnt lgkmcnt(0)
	v_add_f32_e32 v90, v100, v90
	s_waitcnt lgkmcnt(0)
	v_add_f32_e32 v92, v99, v92
	s_waitcnt lgkmcnt(0)
	v_add_f32_e32 v94, v96, v94
	v_cndmask_b32_e64 v96, v90, v95, s[12:13]
	v_cndmask_b32_e64 v90, v95, v90, s[12:13]
	s_nop 1
	v_mov_b32_dpp v90, v90 row_ror:8 row_mask:0xf bank_mask:0xf
	v_cndmask_b32_e64 v95, v94, v92, s[14:15]
	v_cndmask_b32_e64 v92, v92, v94, s[14:15]
	s_nop 1
	v_mov_b32_dpp v92, v92 row_half_mirror row_mask:0xf bank_mask:0xf
	s_nop 1
	v_mov_b32_dpp v92, v92 quad_perm:[3,2,1,0] row_mask:0xf bank_mask:0xf
	s_waitcnt lgkmcnt(0)
	v_add_f32_e32 v90, v96, v90
	v_cndmask_b32_e64 v94, v90, v93, s[14:15]
	v_cndmask_b32_e64 v90, v93, v90, s[14:15]
	s_nop 1
	v_mov_b32_dpp v90, v90 row_half_mirror row_mask:0xf bank_mask:0xf
	s_nop 1
	v_mov_b32_dpp v90, v90 quad_perm:[3,2,1,0] row_mask:0xf bank_mask:0xf
	s_waitcnt lgkmcnt(0)
	v_add_f32_e32 v92, v95, v92
	s_waitcnt lgkmcnt(0)
	v_add_f32_e32 v90, v94, v90
	v_cndmask_b32_e64 v93, v90, v92, s[16:17]
	v_cndmask_b32_e64 v90, v92, v90, s[16:17]
	s_nop 1
	v_mov_b32_dpp v90, v90 quad_perm:[2,3,0,1] row_mask:0xf bank_mask:0xf
	s_waitcnt lgkmcnt(0)
	v_add_f32_e32 v90, v93, v90
	s_nop 1
	v_permlane32_swap_b32_e32 v175, v217
	s_nop 1
	v_permlane32_swap_b32_e32 v176, v219
	s_nop 1
	v_permlane32_swap_b32_e32 v177, v220
	s_nop 1
	v_permlane32_swap_b32_e32 v179, v222
	s_nop 1
	v_permlane32_swap_b32_e32 v181, v224
	s_nop 1
	v_permlane32_swap_b32_e32 v183, v226
	s_nop 1
	v_permlane32_swap_b32_e32 v185, v228
	s_nop 1
	v_permlane32_swap_b32_e32 v187, v230
	s_nop 1
	v_mov_b32_dpp v92, v90 quad_perm:[1,0,3,2] row_mask:0xf bank_mask:0xf
	s_nop 1
	v_permlane32_swap_b32_e32 v189, v232
	s_nop 1
	v_permlane32_swap_b32_e32 v191, v234
	s_waitcnt lgkmcnt(0)
	v_add_f32_e32 v90, v90, v92
	v_add_f32_e32 v92, v122, v90
	v_add_f32_e32 v90, v175, v217
	v_permlane32_swap_b32_e32 v193, v236
	v_add_f32_e32 v93, v176, v219
	v_add_f32_e32 v94, v177, v220
	v_add_f32_e32 v95, v179, v222
	v_permlane32_swap_b32_e32 v195, v238
	v_add_f32_e32 v96, v181, v224
	v_add_f32_e32 v97, v183, v226
	v_add_f32_e32 v98, v185, v228
	v_permlane32_swap_b32_e32 v197, v240
	v_add_f32_e32 v99, v187, v230
	v_add_f32_e32 v100, v189, v232
	v_add_f32_e32 v101, v191, v234
	v_permlane32_swap_b32_e32 v199, v242
	v_add_f32_e32 v102, v193, v236
	v_add_f32_e32 v103, v195, v238
	v_add_f32_e32 v104, v197, v240
	v_permlane32_swap_b32_e32 v209, v244
	v_add_f32_e32 v105, v199, v242
	v_add_f32_e32 v106, v209, v244
	v_cndmask_b32_e64 v107, v91, v214, s[8:9]
	v_cndmask_b32_e64 v91, v214, v91, s[8:9]
	v_mov_b32_e32 v108, v91
	s_nop 1
	v_permlane32_swap_b32_e32 v91, v108
	v_cndmask_b32_e64 v91, v91, v108, s[8:9]
	v_add_f32_e32 v91, v107, v91
	v_cndmask_b32_e64 v107, v100, v90, s[10:11]
	v_cndmask_b32_e64 v90, v90, v100, s[10:11]
	v_permlane16_swap_b32_e32 v93, v101
	ds_swizzle_b32 v90, v90 offset:swizzle(SWAP,16)
	s_waitcnt lgkmcnt(1)
	v_add_f32_e32 v93, v93, v101
	v_permlane16_swap_b32_e32 v94, v102
	s_waitcnt lgkmcnt(0)
	v_add_f32_e32 v90, v107, v90
	s_waitcnt lgkmcnt(0)
	v_add_f32_e32 v94, v94, v102
	v_permlane16_swap_b32_e32 v95, v103
	s_waitcnt lgkmcnt(0)
	v_add_f32_e32 v95, v95, v103
	v_permlane16_swap_b32_e32 v96, v104
	s_waitcnt lgkmcnt(0)
	v_add_f32_e32 v96, v96, v104
	v_permlane16_swap_b32_e32 v97, v105
	s_waitcnt lgkmcnt(0)
	v_add_f32_e32 v97, v97, v105
	v_permlane16_swap_b32_e32 v98, v106
	s_waitcnt lgkmcnt(0)
	v_add_f32_e32 v98, v98, v106
	v_cndmask_b32_e64 v100, v91, v99, s[10:11]
	v_cndmask_b32_e64 v91, v99, v91, s[10:11]
	v_cndmask_b32_e64 v99, v96, v90, s[12:13]
	v_cndmask_b32_e64 v90, v90, v96, s[12:13]
	v_cndmask_b32_e64 v96, v97, v93, s[12:13]
	v_cndmask_b32_e64 v93, v93, v97, s[12:13]
	s_nop 1
	v_mov_b32_dpp v93, v93 row_ror:8 row_mask:0xf bank_mask:0xf
	ds_swizzle_b32 v91, v91 offset:swizzle(SWAP,16)
	s_nop 1
	v_mov_b32_dpp v90, v90 row_ror:8 row_mask:0xf bank_mask:0xf
	s_waitcnt lgkmcnt(1)
	v_add_f32_e32 v93, v96, v93
	v_cndmask_b32_e64 v96, v98, v94, s[12:13]
	v_cndmask_b32_e64 v94, v94, v98, s[12:13]
	s_nop 1
	v_mov_b32_dpp v94, v94 row_ror:8 row_mask:0xf bank_mask:0xf
	s_waitcnt lgkmcnt(0)
	v_add_f32_e32 v91, v100, v91
	s_waitcnt lgkmcnt(0)
	v_add_f32_e32 v90, v99, v90
	s_waitcnt lgkmcnt(0)
	v_add_f32_e32 v94, v96, v94
	v_cndmask_b32_e64 v96, v91, v95, s[12:13]
	v_cndmask_b32_e64 v91, v95, v91, s[12:13]
	s_nop 1
	v_mov_b32_dpp v91, v91 row_ror:8 row_mask:0xf bank_mask:0xf
	v_cndmask_b32_e64 v95, v94, v90, s[14:15]
	v_cndmask_b32_e64 v90, v90, v94, s[14:15]
	s_nop 1
	v_mov_b32_dpp v90, v90 row_half_mirror row_mask:0xf bank_mask:0xf
	s_nop 1
	v_mov_b32_dpp v90, v90 quad_perm:[3,2,1,0] row_mask:0xf bank_mask:0xf
	s_waitcnt lgkmcnt(0)
	v_add_f32_e32 v91, v96, v91
	v_cndmask_b32_e64 v94, v91, v93, s[14:15]
	v_cndmask_b32_e64 v91, v93, v91, s[14:15]
	s_nop 1
	v_mov_b32_dpp v91, v91 row_half_mirror row_mask:0xf bank_mask:0xf
	s_nop 1
	v_mov_b32_dpp v91, v91 quad_perm:[3,2,1,0] row_mask:0xf bank_mask:0xf
	s_waitcnt lgkmcnt(0)
	v_add_f32_e32 v90, v95, v90
	s_waitcnt lgkmcnt(0)
	v_add_f32_e32 v91, v94, v91
	v_cndmask_b32_e64 v93, v91, v90, s[16:17]
	v_cndmask_b32_e64 v90, v90, v91, s[16:17]
	s_nop 1
	v_mov_b32_dpp v90, v90 quad_perm:[2,3,0,1] row_mask:0xf bank_mask:0xf
	s_waitcnt lgkmcnt(0)
	v_add_f32_e32 v93, v93, v90
	s_nop 1
	v_mov_b32_dpp v94, v93 quad_perm:[1,0,3,2] row_mask:0xf bank_mask:0xf
	s_and_saveexec_b64 s[84:85], s[18:19]
	ds_write_b32 v127, v92
	s_or_b64 exec, exec, s[84:85]
	s_waitcnt lgkmcnt(0)
	v_mov_b32_e32 v90, s4
	ds_read_b128 v[96:99], v90
	ds_read_b128 v[100:103], v90 offset:16
	ds_read_b128 v[104:107], v90 offset:32
	ds_read_b128 v[108:111], v90 offset:48
	s_waitcnt lgkmcnt(3)
	v_cmp_eq_f32_e64 s[84:85], v96, v92
	v_cmp_gt_f32_e32 vcc, v96, v92
	s_and_b64 s[84:85], s[84:85], s[20:21]
	s_or_b64 s[84:85], vcc, s[84:85]
	v_cndmask_b32_e64 v91, 0, 1, s[84:85]
	v_cmp_eq_f32_e64 s[84:85], v97, v92
	v_cmp_gt_f32_e32 vcc, v97, v92
	s_and_b64 s[84:85], s[84:85], s[22:23]
	s_or_b64 s[84:85], vcc, s[84:85]
	v_cndmask_b32_e64 v95, 0, 1, s[84:85]
	v_cmp_eq_f32_e64 s[84:85], v98, v92
	v_cmp_gt_f32_e32 vcc, v98, v92
	s_and_b64 s[84:85], s[84:85], s[24:25]
	s_or_b64 s[84:85], vcc, s[84:85]
	v_cndmask_b32_e64 v96, 0, 1, s[84:85]
	v_cmp_eq_f32_e64 s[84:85], v99, v92
	v_cmp_gt_f32_e32 vcc, v99, v92
	s_and_b64 s[84:85], s[84:85], s[26:27]
	s_or_b64 s[84:85], vcc, s[84:85]
	v_add3_u32 v91, v91, v95, v96
	v_cndmask_b32_e64 v95, 0, 1, s[84:85]
	s_waitcnt lgkmcnt(2)
	v_cmp_eq_f32_e64 s[84:85], v100, v92
	v_cmp_gt_f32_e32 vcc, v100, v92
	s_and_b64 s[84:85], s[84:85], s[28:29]
	s_or_b64 s[84:85], vcc, s[84:85]
	v_cndmask_b32_e64 v96, 0, 1, s[84:85]
	v_cmp_eq_f32_e64 s[84:85], v101, v92
	v_cmp_gt_f32_e32 vcc, v101, v92
	s_and_b64 s[84:85], s[84:85], s[30:31]
	s_or_b64 s[84:85], vcc, s[84:85]
	v_add3_u32 v91, v91, v95, v96
	v_cndmask_b32_e64 v95, 0, 1, s[84:85]
	v_cmp_eq_f32_e64 s[84:85], v102, v92
	v_cmp_gt_f32_e32 vcc, v102, v92
	s_and_b64 s[84:85], s[84:85], s[34:35]
	s_or_b64 s[84:85], vcc, s[84:85]
	v_cndmask_b32_e64 v96, 0, 1, s[84:85]
	v_cmp_eq_f32_e64 s[84:85], v103, v92
	v_cmp_gt_f32_e32 vcc, v103, v92
	s_and_b64 s[84:85], s[84:85], s[38:39]
	s_or_b64 s[84:85], vcc, s[84:85]
	v_add3_u32 v91, v91, v95, v96
	v_cndmask_b32_e64 v95, 0, 1, s[84:85]
	s_waitcnt lgkmcnt(1)
	v_cmp_eq_f32_e64 s[84:85], v104, v92
	v_cmp_gt_f32_e32 vcc, v104, v92
	s_and_b64 s[84:85], s[84:85], s[40:41]
	s_or_b64 s[84:85], vcc, s[84:85]
	v_cndmask_b32_e64 v96, 0, 1, s[84:85]
	v_cmp_eq_f32_e64 s[84:85], v105, v92
	v_cmp_gt_f32_e32 vcc, v105, v92
	s_and_b64 s[84:85], s[84:85], s[42:43]
	s_or_b64 s[84:85], vcc, s[84:85]
	v_add3_u32 v91, v91, v95, v96
	v_cndmask_b32_e64 v95, 0, 1, s[84:85]
	v_cmp_eq_f32_e64 s[84:85], v106, v92
	v_cmp_gt_f32_e32 vcc, v106, v92
	s_and_b64 s[84:85], s[84:85], s[44:45]
	s_or_b64 s[84:85], vcc, s[84:85]
	v_cndmask_b32_e64 v96, 0, 1, s[84:85]
	v_cmp_eq_f32_e64 s[84:85], v107, v92
	v_cmp_gt_f32_e32 vcc, v107, v92
	s_and_b64 s[84:85], s[84:85], s[46:47]
	s_or_b64 s[84:85], vcc, s[84:85]
	v_add3_u32 v91, v91, v95, v96
	v_cndmask_b32_e64 v95, 0, 1, s[84:85]
	s_waitcnt lgkmcnt(0)
	v_cmp_eq_f32_e64 s[84:85], v108, v92
	v_cmp_gt_f32_e32 vcc, v108, v92
	s_and_b64 s[84:85], s[84:85], s[48:49]
	s_or_b64 s[84:85], vcc, s[84:85]
	v_cndmask_b32_e64 v96, 0, 1, s[84:85]
	v_cmp_eq_f32_e64 s[84:85], v109, v92
	v_cmp_gt_f32_e32 vcc, v109, v92
	s_and_b64 s[84:85], s[84:85], s[50:51]
	s_or_b64 s[84:85], vcc, s[84:85]
	v_add3_u32 v91, v91, v95, v96
	v_cndmask_b32_e64 v95, 0, 1, s[84:85]
	v_cmp_eq_f32_e64 s[84:85], v110, v92
	v_cmp_gt_f32_e32 vcc, v110, v92
	s_and_b64 s[84:85], s[84:85], s[86:87]
	s_or_b64 s[84:85], vcc, s[84:85]
	v_cndmask_b32_e64 v96, 0, 1, s[84:85]
	v_add3_u32 v91, v91, v95, v96
	ds_read_b128 v[96:99], v90 offset:64
	ds_read_b128 v[100:103], v90 offset:80
	v_cmp_eq_f32_e64 s[84:85], v111, v92
	v_cmp_gt_f32_e32 vcc, v111, v92
	s_and_b64 s[84:85], s[84:85], s[52:53]
	s_or_b64 s[84:85], vcc, s[84:85]
	v_cndmask_b32_e64 v95, 0, 1, s[84:85]
	s_waitcnt lgkmcnt(1)
	v_cmp_eq_f32_e64 s[84:85], v96, v92
	v_cmp_gt_f32_e32 vcc, v96, v92
	s_and_b64 s[84:85], s[84:85], s[54:55]
	s_or_b64 s[84:85], vcc, s[84:85]
	v_cndmask_b32_e64 v96, 0, 1, s[84:85]
	v_cmp_eq_f32_e64 s[84:85], v97, v92
	v_cmp_gt_f32_e32 vcc, v97, v92
	s_and_b64 s[84:85], s[84:85], s[56:57]
	s_or_b64 s[84:85], vcc, s[84:85]
	v_add3_u32 v91, v91, v95, v96
	v_cndmask_b32_e64 v95, 0, 1, s[84:85]
	v_cmp_eq_f32_e64 s[84:85], v98, v92
	v_cmp_gt_f32_e32 vcc, v98, v92
	s_and_b64 s[84:85], s[84:85], s[58:59]
	s_or_b64 s[84:85], vcc, s[84:85]
	v_cndmask_b32_e64 v96, 0, 1, s[84:85]
	v_cmp_eq_f32_e64 s[84:85], v99, v92
	v_cmp_gt_f32_e32 vcc, v99, v92
	s_and_b64 s[84:85], s[84:85], s[60:61]
	s_or_b64 s[84:85], vcc, s[84:85]
	v_add3_u32 v91, v91, v95, v96
	v_cndmask_b32_e64 v95, 0, 1, s[84:85]
	s_waitcnt lgkmcnt(0)
	v_cmp_eq_f32_e64 s[84:85], v100, v92
	v_cmp_gt_f32_e32 vcc, v100, v92
	s_and_b64 s[84:85], s[84:85], s[62:63]
	s_or_b64 s[84:85], vcc, s[84:85]
	v_cndmask_b32_e64 v96, 0, 1, s[84:85]
	v_cmp_eq_f32_e64 s[84:85], v101, v92
	v_cmp_gt_f32_e32 vcc, v101, v92
	s_and_b64 s[84:85], s[84:85], s[64:65]
	s_or_b64 s[84:85], vcc, s[84:85]
	v_add3_u32 v91, v91, v95, v96
	v_cndmask_b32_e64 v95, 0, 1, s[84:85]
	v_cmp_eq_f32_e64 s[84:85], v102, v92
	v_cmp_gt_f32_e32 vcc, v102, v92
	s_and_b64 s[84:85], s[84:85], s[66:67]
	s_or_b64 s[84:85], vcc, s[84:85]
	v_cndmask_b32_e64 v96, 0, 1, s[84:85]
	v_add3_u32 v91, v91, v95, v96
	ds_read_b128 v[96:99], v90 offset:96
	v_cmp_eq_f32_e64 s[84:85], v103, v92
	v_cmp_gt_f32_e32 vcc, v103, v92
	s_and_b64 s[84:85], s[84:85], s[68:69]
	s_or_b64 s[84:85], vcc, s[84:85]
	v_cndmask_b32_e64 v95, 0, 1, s[84:85]
	ds_read_b128 v[100:103], v90 offset:112
	s_waitcnt lgkmcnt(1)
	v_cmp_eq_f32_e64 s[84:85], v96, v92
	v_cmp_gt_f32_e32 vcc, v96, v92
	s_and_b64 s[84:85], s[84:85], s[70:71]
	s_or_b64 s[84:85], vcc, s[84:85]
	v_cndmask_b32_e64 v90, 0, 1, s[84:85]
	v_cmp_eq_f32_e64 s[84:85], v97, v92
	v_cmp_gt_f32_e32 vcc, v97, v92
	s_and_b64 s[84:85], s[84:85], s[72:73]
	s_or_b64 s[84:85], vcc, s[84:85]
	v_cndmask_b32_e64 v96, 0, 1, s[84:85]
	v_cmp_eq_f32_e64 s[84:85], v98, v92
	v_cmp_gt_f32_e32 vcc, v98, v92
	s_and_b64 s[84:85], s[84:85], s[74:75]
	s_or_b64 s[84:85], vcc, s[84:85]
	v_cndmask_b32_e64 v97, 0, 1, s[84:85]
	v_cmp_eq_f32_e64 s[84:85], v99, v92
	v_cmp_gt_f32_e32 vcc, v99, v92
	s_and_b64 s[84:85], s[84:85], s[76:77]
	s_or_b64 s[84:85], vcc, s[84:85]
	v_cndmask_b32_e64 v98, 0, 1, s[84:85]
	s_waitcnt lgkmcnt(0)
	v_cmp_eq_f32_e64 s[84:85], v100, v92
	v_cmp_gt_f32_e32 vcc, v100, v92
	s_and_b64 s[84:85], s[84:85], s[78:79]
	s_or_b64 s[84:85], vcc, s[84:85]
	v_cndmask_b32_e64 v99, 0, 1, s[84:85]
	v_cmp_eq_f32_e64 s[84:85], v101, v92
	v_cmp_gt_f32_e32 vcc, v101, v92
	s_and_b64 s[84:85], s[84:85], s[80:81]
	s_or_b64 s[84:85], vcc, s[84:85]
	v_cndmask_b32_e64 v100, 0, 1, s[84:85]
	v_cmp_eq_f32_e64 s[84:85], v102, v92
	v_cmp_gt_f32_e32 vcc, v102, v92
	s_and_b64 s[84:85], s[82:83], s[84:85]
	s_or_b64 s[84:85], vcc, s[84:85]
	v_cmp_gt_f32_e32 vcc, v103, v92
	v_cndmask_b32_e64 v101, 0, 1, s[84:85]
	s_nop 0
	v_addc_co_u32_e32 v91, vcc, v91, v95, vcc
	v_add_u32_e32 v90, v91, v90
	v_add3_u32 v90, v90, v96, v97
	v_add3_u32 v90, v90, v98, v99
	v_add3_u32 v90, v90, v100, v101
	v_cmp_gt_u32_e32 vcc, 4, v90
	s_and_b64 vcc, s[0:1], vcc
	s_and_saveexec_b64 s[84:85], vcc
	v_lshl_add_u32 v91, v90, 2, s4
	ds_write_b32 v91, v92 offset:128
	s_or_b64 exec, exec, s[84:85]
	s_waitcnt lgkmcnt(0)
	s_and_saveexec_b64 s[84:85], vcc
	s_cbranch_execz .LBB0_773
	v_mov_b32_e32 v91, s4
	ds_read_b128 v[96:99], v91 offset:128
	s_waitcnt lgkmcnt(0)
	v_sub_f32_e32 v91, v97, v96
	v_sub_f32_e32 v95, v98, v96
	v_mul_f32_e32 v91, 0x3fb8aa3b, v91
	v_sub_f32_e32 v97, v99, v96
	v_mul_f32_e32 v95, 0x3fb8aa3b, v95
	v_exp_f32_e32 v91, v91
	v_mul_f32_e32 v97, 0x3fb8aa3b, v97
	v_exp_f32_e32 v95, v95
	v_exp_f32_e32 v97, v97
	v_add_f32_e32 v91, 1.0, v91
	v_sub_f32_e32 v92, v92, v96
	v_add_f32_e32 v91, v95, v91
	v_add_f32_e32 v91, v97, v91
	v_div_scale_f32 v95, s[92:93], v91, v91, 1.0
	v_rcp_f32_e32 v97, v95
	v_div_scale_f32 v98, vcc, 1.0, v91, 1.0
	s_lshl_b64 s[92:93], s[96:97], 4
	v_fma_f32 v99, -v95, v97, 1.0
	v_fmac_f32_e32 v97, v99, v97
	v_mul_f32_e32 v99, v98, v97
	v_fma_f32 v100, -v95, v99, v98
	v_fmac_f32_e32 v99, v100, v97
	v_fma_f32 v95, -v95, v99, v98
	v_div_fmas_f32 v95, v95, v97, v99
	v_div_fixup_f32 v95, v95, v91, 1.0
	v_mov_b32_e32 v91, v201
	v_lshlrev_b64 v[90:91], 2, v[90:91]
	v_mul_f32_e32 v92, 0x3fb8aa3b, v92
	v_or_b32_e32 v91, s93, v91
	v_exp_f32_e32 v92, v92
	v_or_b32_e32 v90, s92, v90
	v_readlane_b32 s92, v254, 45
	v_readlane_b32 s93, v254, 46
	v_mul_f32_e32 v92, v92, v95
	s_nop 0
	v_lshl_add_u64 v[96:97], s[92:93], 0, v[90:91]
	v_readlane_b32 s92, v254, 43
	v_readlane_b32 s93, v254, 44
	global_store_dword v[96:97], v126, off
	s_nop 0
	v_lshl_add_u64 v[90:91], s[92:93], 0, v[90:91]
	global_store_dword v[90:91], v92, off
	v_mov_b32_e32 v90, 1
	ds_add_u32 v128, v90
